# speedup vs baseline: 1.0283x; 1.0283x over previous
.LBB0_78:
	s_load_dwordx2 s[0:1], s[0:1], 0x28
	v_lshlrev_b32_e32 v2, 9, v0
	v_and_b32_e32 v13, 3, v0
	v_and_b32_e32 v2, 0x7800, v2
	v_mov_b32_e32 v3, 0
	v_lshl_or_b32 v12, s36, 2, v13
	s_waitcnt lgkmcnt(0)
	s_mov_b64 s[44:45], s[0:1]
	v_lshl_add_u64 v[4:5], s[0:1], 0, v[2:3]
	s_lshl_b32 s0, s33, 7
	v_lshl_or_b32 v2, v12, 3, s0
	v_lshl_add_u64 v[10:11], v[4:5], 0, v[2:3]
	v_and_b32_e32 v160, 15, v0
	v_bfe_u32 v161, v0, 4, 2
	s_and_b32 s46, s36, 1
	s_lshl_b32 s46, s46, 5
	v_lshl_add_u32 v162, v161, 3, s46
	v_lshlrev_b32_e32 v162, 7, v162
	s_lshl_b32 s47, s33, 5
	s_lshr_b32 s46, s36, 1
	s_add_i32 s47, s47, s46
	v_lshl_add_u32 v163, v160, 1, s47
	v_add_lshl_u32 v162, v162, v163, 2
	global_load_dword v152, v162, s[44:45]
	global_load_dword v153, v162, s[44:45] offset:512
	global_load_dword v154, v162, s[44:45] offset:1024
	global_load_dword v155, v162, s[44:45] offset:1536
	global_load_dword v156, v162, s[44:45] offset:2048
	global_load_dword v157, v162, s[44:45] offset:2560
	global_load_dword v158, v162, s[44:45] offset:3072
	global_load_dword v159, v162, s[44:45] offset:3584
	s_bfe_u32 s5, s2, 0x30002
	s_mov_b32 s4, 2
	s_cmp_gt_u32 s5, 3
	v_lshlrev_b32_e32 v10, 2, v0
	s_cbranch_scc0 .LBB0_80
	v_and_b32_e32 v11, 16, v10
	v_lshl_or_b32 v14, s5, 5, v11
	s_cbranch_execz .LBB0_81
	s_branch .LBB0_82

.LBB0_86:
	s_or_b64 exec, exec, s[0:1]
	v_cmp_ne_u32_e32 vcc, 0, v14
	s_waitcnt lgkmcnt(0)
	s_barrier
	s_setprio 2
	v_and_b32_e32 v40, 15, v1
	v_lshrrev_b32_e32 v41, 4, v1
	s_and_b32 s44, s36, 1
	s_lshr_b32 s45, s36, 1
	s_mov_b32 s60, 0xffff
	s_mov_b32 s61, 0
	s_mov_b32 s62, 0xffff0000
	s_mov_b32 s63, 0
	s_mov_b32 s64, 0
	s_mov_b32 s65, 0xffff
	s_mov_b32 s66, 0
	s_mov_b32 s67, 0xffff0000
	v_cvt_pk_f16_f32 v2, v152, v153
	v_cvt_pk_f16_f32 v3, v154, v155
	v_cvt_pk_f16_f32 v4, v156, v157
	v_cvt_pk_f16_f32 v5, v158, v159
	s_lshl_b32 s46, s44, 3
	v_lshl_add_u32 v42, v41, 1, s46
	v_mul_u32_u24_e32 v32, 0x650, v42
	v_lshl_add_u32 v34, v40, 3, v32
	v_mul_u32_u24_e32 v33, 0x650, v40
	v_add_u32_e32 v33, 0x6500, v33
	s_lshl_b32 s47, s45, 1
	v_lshl_add_u32 v35, v40, 2, s47
	v_lshl_add_u32 v35, v41, 8, v35
	s_lshl_b32 s46, s3, 2
	s_add_i32 s46, s46, s33
	s_lshl_b32 s46, s46, 1
	s_add_i32 s46, s46, s44
	s_mul_i32 s46, s46, 0x3200
	s_add_u32 s68, s26, s46
	s_addc_u32 s69, s27, 0
	v_mov_b32_e32 v36, 0x14a00
.Lc_wait0:
	ds_read_b32 v37, v36
	ds_read_b32 v38, v36 offset:64
	s_waitcnt lgkmcnt(0)
	v_readfirstlane_b32 s4, v37
	v_readfirstlane_b32 s5, v38
	s_and_b32 s4, s4, s5
	s_cbranch_scc1 .Lc_go
	s_sleep 1
	s_branch .Lc_wait0
.Lc_go:
	s_cmp_eq_u32 s45, 0
	s_cbranch_scc0 .Lc_par1
	ds_read2_b64 v[48:51], v32 offset0:0 offset1:202
	ds_read_b128 v[120:123], v33 offset:0
	ds_read2_b64 v[10:13], v34 offset0:0 offset1:202
	ds_read2_b64 v[52:55], v32 offset0:1 offset1:203
	ds_read2_b64 v[56:59], v32 offset0:2 offset1:204
	ds_read_b128 v[124:127], v33 offset:16
	ds_read2_b64 v[60:63], v32 offset0:3 offset1:205
	ds_read2_b64 v[64:67], v32 offset0:4 offset1:206
	ds_read_b128 v[128:131], v33 offset:32
	ds_read2_b64 v[68:71], v32 offset0:5 offset1:207
	s_mov_b32 s70, 0
.Lc0_loop:
	s_waitcnt lgkmcnt(6)
	v_pk_fma_f16 v6, v2, v120, v121 op_sel:[0,0,0] op_sel_hi:[1,0,0] neg_lo:[1,0,0] neg_hi:[1,0,0]
	v_pk_fma_f16 v7, v3, v120, v121 op_sel:[0,0,0] op_sel_hi:[1,0,0] neg_lo:[1,0,0] neg_hi:[1,0,0]
	v_pk_fma_f16 v8, v4, v120, v121 op_sel:[0,0,0] op_sel_hi:[1,0,0] neg_lo:[1,0,0] neg_hi:[1,0,0]
	v_pk_fma_f16 v9, v5, v120, v121 op_sel:[0,0,0] op_sel_hi:[1,0,0] neg_lo:[1,0,0] neg_hi:[1,0,0]
	v_mfma_f32_16x16x32_f16 v[18:21], v[10:13], v[2:5], 0
	ds_read2_b64 v[72:75], v32 offset0:6 offset1:208
	ds_read_b128 v[132:135], v33 offset:48
	ds_read_b32 v37, v36 offset:4
	ds_read_b32 v38, v36 offset:68
	v_pk_fma_f16 v2, v48, v6, v2
	v_pk_fma_f16 v3, v49, v7, v3
	v_pk_fma_f16 v4, v50, v8, v4
	v_pk_fma_f16 v5, v51, v9, v5
	v_cndmask_b32_e64 v29, v29, v25, s[66:67]
	s_cmp_eq_u32 s70, 0
	s_cbranch_scc1 .Lc0_nost
	v_cvt_pk_f16_f32 v30, v26, v27
	v_cvt_pk_f16_f32 v31, v28, v29
	global_store_short v35, v30, s[68:69]
	global_store_short_d16_hi v35, v30, s[68:69] offset:64
	global_store_short v35, v31, s[68:69] offset:128
	global_store_short_d16_hi v35, v31, s[68:69] offset:192
	v_add_u32_e32 v35, 0x400, v35
.Lc0_nost:
	v_pk_fma_f16 v6, v2, v122, v123 op_sel:[0,0,0] op_sel_hi:[1,0,0] neg_lo:[1,0,0] neg_hi:[1,0,0]
	v_pk_fma_f16 v7, v3, v122, v123 op_sel:[0,0,0] op_sel_hi:[1,0,0] neg_lo:[1,0,0] neg_hi:[1,0,0]
	v_pk_fma_f16 v8, v4, v122, v123 op_sel:[0,0,0] op_sel_hi:[1,0,0] neg_lo:[1,0,0] neg_hi:[1,0,0]
	v_pk_fma_f16 v9, v5, v122, v123 op_sel:[0,0,0] op_sel_hi:[1,0,0] neg_lo:[1,0,0] neg_hi:[1,0,0]
	v_mfma_f32_16x16x32_f16 v[22:25], v[10:13], v[2:5], 0
	ds_read2_b64 v[76:79], v32 offset0:7 offset1:209
	v_pk_fma_f16 v2, v52, v6, v2
	v_pk_fma_f16 v3, v53, v7, v3
	v_pk_fma_f16 v4, v54, v8, v4
	v_pk_fma_f16 v5, v55, v9, v5
	v_cndmask_b32_e64 v26, v26, v18, s[60:61]
	s_waitcnt lgkmcnt(8)
	v_pk_fma_f16 v6, v2, v124, v125 op_sel:[0,0,0] op_sel_hi:[1,0,0] neg_lo:[1,0,0] neg_hi:[1,0,0]
	v_pk_fma_f16 v7, v3, v124, v125 op_sel:[0,0,0] op_sel_hi:[1,0,0] neg_lo:[1,0,0] neg_hi:[1,0,0]
	v_pk_fma_f16 v8, v4, v124, v125 op_sel:[0,0,0] op_sel_hi:[1,0,0] neg_lo:[1,0,0] neg_hi:[1,0,0]
	v_pk_fma_f16 v9, v5, v124, v125 op_sel:[0,0,0] op_sel_hi:[1,0,0] neg_lo:[1,0,0] neg_hi:[1,0,0]
	v_mfma_f32_16x16x32_f16 v[18:21], v[10:13], v[2:5], 0
	ds_read2_b64 v[80:83], v32 offset0:8 offset1:210
	ds_read_b128 v[136:139], v33 offset:64
	v_pk_fma_f16 v2, v56, v6, v2
	v_pk_fma_f16 v3, v57, v7, v3
	v_pk_fma_f16 v4, v58, v8, v4
	v_pk_fma_f16 v5, v59, v9, v5
	v_cndmask_b32_e64 v27, v27, v23, s[60:61]
	v_pk_fma_f16 v6, v2, v126, v127 op_sel:[0,0,0] op_sel_hi:[1,0,0] neg_lo:[1,0,0] neg_hi:[1,0,0]
	v_pk_fma_f16 v7, v3, v126, v127 op_sel:[0,0,0] op_sel_hi:[1,0,0] neg_lo:[1,0,0] neg_hi:[1,0,0]
	v_pk_fma_f16 v8, v4, v126, v127 op_sel:[0,0,0] op_sel_hi:[1,0,0] neg_lo:[1,0,0] neg_hi:[1,0,0]
	v_pk_fma_f16 v9, v5, v126, v127 op_sel:[0,0,0] op_sel_hi:[1,0,0] neg_lo:[1,0,0] neg_hi:[1,0,0]
	v_mfma_f32_16x16x32_f16 v[22:25], v[10:13], v[2:5], 0
	ds_read2_b64 v[84:87], v32 offset0:9 offset1:211
	v_pk_fma_f16 v2, v60, v6, v2
	v_pk_fma_f16 v3, v61, v7, v3
	v_pk_fma_f16 v4, v62, v8, v4
	v_pk_fma_f16 v5, v63, v9, v5
	v_cndmask_b32_e64 v28, v28, v20, s[60:61]
	s_waitcnt lgkmcnt(8)
	v_pk_fma_f16 v6, v2, v128, v129 op_sel:[0,0,0] op_sel_hi:[1,0,0] neg_lo:[1,0,0] neg_hi:[1,0,0]
	v_pk_fma_f16 v7, v3, v128, v129 op_sel:[0,0,0] op_sel_hi:[1,0,0] neg_lo:[1,0,0] neg_hi:[1,0,0]
	v_pk_fma_f16 v8, v4, v128, v129 op_sel:[0,0,0] op_sel_hi:[1,0,0] neg_lo:[1,0,0] neg_hi:[1,0,0]
	v_pk_fma_f16 v9, v5, v128, v129 op_sel:[0,0,0] op_sel_hi:[1,0,0] neg_lo:[1,0,0] neg_hi:[1,0,0]
	v_mfma_f32_16x16x32_f16 v[18:21], v[10:13], v[2:5], 0
	ds_read2_b64 v[88:91], v32 offset0:10 offset1:212
	ds_read_b128 v[140:143], v33 offset:80
	v_pk_fma_f16 v2, v64, v6, v2
	v_pk_fma_f16 v3, v65, v7, v3
	v_pk_fma_f16 v4, v66, v8, v4
	v_pk_fma_f16 v5, v67, v9, v5
	v_cndmask_b32_e64 v29, v29, v25, s[60:61]
	v_pk_fma_f16 v6, v2, v130, v131 op_sel:[0,0,0] op_sel_hi:[1,0,0] neg_lo:[1,0,0] neg_hi:[1,0,0]
	v_pk_fma_f16 v7, v3, v130, v131 op_sel:[0,0,0] op_sel_hi:[1,0,0] neg_lo:[1,0,0] neg_hi:[1,0,0]
	v_pk_fma_f16 v8, v4, v130, v131 op_sel:[0,0,0] op_sel_hi:[1,0,0] neg_lo:[1,0,0] neg_hi:[1,0,0]
	v_pk_fma_f16 v9, v5, v130, v131 op_sel:[0,0,0] op_sel_hi:[1,0,0] neg_lo:[1,0,0] neg_hi:[1,0,0]
	v_mfma_f32_16x16x32_f16 v[22:25], v[10:13], v[2:5], 0
	ds_read2_b64 v[92:95], v32 offset0:11 offset1:213
	v_pk_fma_f16 v2, v68, v6, v2
	v_pk_fma_f16 v3, v69, v7, v3
	v_pk_fma_f16 v4, v70, v8, v4
	v_pk_fma_f16 v5, v71, v9, v5
	v_cndmask_b32_e64 v26, v26, v18, s[62:63]
	s_waitcnt lgkmcnt(6)
	v_pk_fma_f16 v6, v2, v132, v133 op_sel:[0,0,0] op_sel_hi:[1,0,0] neg_lo:[1,0,0] neg_hi:[1,0,0]
	v_pk_fma_f16 v7, v3, v132, v133 op_sel:[0,0,0] op_sel_hi:[1,0,0] neg_lo:[1,0,0] neg_hi:[1,0,0]
	v_pk_fma_f16 v8, v4, v132, v133 op_sel:[0,0,0] op_sel_hi:[1,0,0] neg_lo:[1,0,0] neg_hi:[1,0,0]
	v_pk_fma_f16 v9, v5, v132, v133 op_sel:[0,0,0] op_sel_hi:[1,0,0] neg_lo:[1,0,0] neg_hi:[1,0,0]
	v_mfma_f32_16x16x32_f16 v[18:21], v[10:13], v[2:5], 0
	ds_read2_b64 v[96:99], v32 offset0:12 offset1:214
	ds_read_b128 v[144:147], v33 offset:96
	v_pk_fma_f16 v2, v72, v6, v2
	v_pk_fma_f16 v3, v73, v7, v3
	v_pk_fma_f16 v4, v74, v8, v4
	v_pk_fma_f16 v5, v75, v9, v5
	v_cndmask_b32_e64 v27, v27, v23, s[62:63]
	v_pk_fma_f16 v6, v2, v134, v135 op_sel:[0,0,0] op_sel_hi:[1,0,0] neg_lo:[1,0,0] neg_hi:[1,0,0]
	v_pk_fma_f16 v7, v3, v134, v135 op_sel:[0,0,0] op_sel_hi:[1,0,0] neg_lo:[1,0,0] neg_hi:[1,0,0]
	v_pk_fma_f16 v8, v4, v134, v135 op_sel:[0,0,0] op_sel_hi:[1,0,0] neg_lo:[1,0,0] neg_hi:[1,0,0]
	v_pk_fma_f16 v9, v5, v134, v135 op_sel:[0,0,0] op_sel_hi:[1,0,0] neg_lo:[1,0,0] neg_hi:[1,0,0]
	v_mfma_f32_16x16x32_f16 v[22:25], v[10:13], v[2:5], 0
	ds_read2_b64 v[100:103], v32 offset0:13 offset1:215
	v_pk_fma_f16 v2, v76, v6, v2
	v_pk_fma_f16 v3, v77, v7, v3
	v_pk_fma_f16 v4, v78, v8, v4
	v_pk_fma_f16 v5, v79, v9, v5
	v_cndmask_b32_e64 v28, v28, v20, s[62:63]
	s_waitcnt lgkmcnt(6)
	v_pk_fma_f16 v6, v2, v136, v137 op_sel:[0,0,0] op_sel_hi:[1,0,0] neg_lo:[1,0,0] neg_hi:[1,0,0]
	v_pk_fma_f16 v7, v3, v136, v137 op_sel:[0,0,0] op_sel_hi:[1,0,0] neg_lo:[1,0,0] neg_hi:[1,0,0]
	v_pk_fma_f16 v8, v4, v136, v137 op_sel:[0,0,0] op_sel_hi:[1,0,0] neg_lo:[1,0,0] neg_hi:[1,0,0]
	v_pk_fma_f16 v9, v5, v136, v137 op_sel:[0,0,0] op_sel_hi:[1,0,0] neg_lo:[1,0,0] neg_hi:[1,0,0]
	v_mfma_f32_16x16x32_f16 v[18:21], v[10:13], v[2:5], 0
	ds_read2_b64 v[104:107], v32 offset0:14 offset1:216
	ds_read_b128 v[148:151], v33 offset:112
	v_pk_fma_f16 v2, v80, v6, v2
	v_pk_fma_f16 v3, v81, v7, v3
	v_pk_fma_f16 v4, v82, v8, v4
	v_pk_fma_f16 v5, v83, v9, v5
	v_cndmask_b32_e64 v29, v29, v25, s[62:63]
	v_readfirstlane_b32 s4, v37
	v_readfirstlane_b32 s5, v38
	s_and_b32 s4, s4, s5
	s_cbranch_scc0 .Lc0_slow0
.Lc0_back0:
	v_pk_fma_f16 v6, v2, v138, v139 op_sel:[0,0,0] op_sel_hi:[1,0,0] neg_lo:[1,0,0] neg_hi:[1,0,0]
	v_pk_fma_f16 v7, v3, v138, v139 op_sel:[0,0,0] op_sel_hi:[1,0,0] neg_lo:[1,0,0] neg_hi:[1,0,0]
	v_pk_fma_f16 v8, v4, v138, v139 op_sel:[0,0,0] op_sel_hi:[1,0,0] neg_lo:[1,0,0] neg_hi:[1,0,0]
	v_pk_fma_f16 v9, v5, v138, v139 op_sel:[0,0,0] op_sel_hi:[1,0,0] neg_lo:[1,0,0] neg_hi:[1,0,0]
	v_mfma_f32_16x16x32_f16 v[22:25], v[10:13], v[2:5], 0
	ds_read2_b64 v[108:111], v32 offset0:15 offset1:217
	v_pk_fma_f16 v2, v84, v6, v2
	v_pk_fma_f16 v3, v85, v7, v3
	v_pk_fma_f16 v4, v86, v8, v4
	v_pk_fma_f16 v5, v87, v9, v5
	v_cndmask_b32_e64 v26, v26, v18, s[64:65]
	s_waitcnt lgkmcnt(6)
	v_pk_fma_f16 v6, v2, v140, v141 op_sel:[0,0,0] op_sel_hi:[1,0,0] neg_lo:[1,0,0] neg_hi:[1,0,0]
	v_pk_fma_f16 v7, v3, v140, v141 op_sel:[0,0,0] op_sel_hi:[1,0,0] neg_lo:[1,0,0] neg_hi:[1,0,0]
	v_pk_fma_f16 v8, v4, v140, v141 op_sel:[0,0,0] op_sel_hi:[1,0,0] neg_lo:[1,0,0] neg_hi:[1,0,0]
	v_pk_fma_f16 v9, v5, v140, v141 op_sel:[0,0,0] op_sel_hi:[1,0,0] neg_lo:[1,0,0] neg_hi:[1,0,0]
	v_mfma_f32_16x16x32_f16 v[18:21], v[10:13], v[2:5], 0
	ds_read2_b64 v[48:51], v32 offset0:16 offset1:218
	ds_read_b128 v[120:123], v33 offset:128
	ds_read2_b64 v[14:17], v34 offset0:16 offset1:218
	v_pk_fma_f16 v2, v88, v6, v2
	v_pk_fma_f16 v3, v89, v7, v3
	v_pk_fma_f16 v4, v90, v8, v4
	v_pk_fma_f16 v5, v91, v9, v5
	v_cndmask_b32_e64 v27, v27, v23, s[64:65]
	v_pk_fma_f16 v6, v2, v142, v143 op_sel:[0,0,0] op_sel_hi:[1,0,0] neg_lo:[1,0,0] neg_hi:[1,0,0]
	v_pk_fma_f16 v7, v3, v142, v143 op_sel:[0,0,0] op_sel_hi:[1,0,0] neg_lo:[1,0,0] neg_hi:[1,0,0]
	v_pk_fma_f16 v8, v4, v142, v143 op_sel:[0,0,0] op_sel_hi:[1,0,0] neg_lo:[1,0,0] neg_hi:[1,0,0]
	v_pk_fma_f16 v9, v5, v142, v143 op_sel:[0,0,0] op_sel_hi:[1,0,0] neg_lo:[1,0,0] neg_hi:[1,0,0]
	v_mfma_f32_16x16x32_f16 v[22:25], v[10:13], v[2:5], 0
	ds_read2_b64 v[52:55], v32 offset0:17 offset1:219
	v_pk_fma_f16 v2, v92, v6, v2
	v_pk_fma_f16 v3, v93, v7, v3
	v_pk_fma_f16 v4, v94, v8, v4
	v_pk_fma_f16 v5, v95, v9, v5
	v_cndmask_b32_e64 v28, v28, v20, s[64:65]
	s_waitcnt lgkmcnt(7)
	v_pk_fma_f16 v6, v2, v144, v145 op_sel:[0,0,0] op_sel_hi:[1,0,0] neg_lo:[1,0,0] neg_hi:[1,0,0]
	v_pk_fma_f16 v7, v3, v144, v145 op_sel:[0,0,0] op_sel_hi:[1,0,0] neg_lo:[1,0,0] neg_hi:[1,0,0]
	v_pk_fma_f16 v8, v4, v144, v145 op_sel:[0,0,0] op_sel_hi:[1,0,0] neg_lo:[1,0,0] neg_hi:[1,0,0]
	v_pk_fma_f16 v9, v5, v144, v145 op_sel:[0,0,0] op_sel_hi:[1,0,0] neg_lo:[1,0,0] neg_hi:[1,0,0]
	v_mfma_f32_16x16x32_f16 v[18:21], v[10:13], v[2:5], 0
	ds_read2_b64 v[56:59], v32 offset0:18 offset1:220
	ds_read_b128 v[124:127], v33 offset:144
	v_pk_fma_f16 v2, v96, v6, v2
	v_pk_fma_f16 v3, v97, v7, v3
	v_pk_fma_f16 v4, v98, v8, v4
	v_pk_fma_f16 v5, v99, v9, v5
	v_cndmask_b32_e64 v29, v29, v25, s[64:65]
	v_pk_fma_f16 v6, v2, v146, v147 op_sel:[0,0,0] op_sel_hi:[1,0,0] neg_lo:[1,0,0] neg_hi:[1,0,0]
	v_pk_fma_f16 v7, v3, v146, v147 op_sel:[0,0,0] op_sel_hi:[1,0,0] neg_lo:[1,0,0] neg_hi:[1,0,0]
	v_pk_fma_f16 v8, v4, v146, v147 op_sel:[0,0,0] op_sel_hi:[1,0,0] neg_lo:[1,0,0] neg_hi:[1,0,0]
	v_pk_fma_f16 v9, v5, v146, v147 op_sel:[0,0,0] op_sel_hi:[1,0,0] neg_lo:[1,0,0] neg_hi:[1,0,0]
	v_mfma_f32_16x16x32_f16 v[22:25], v[10:13], v[2:5], 0
	ds_read2_b64 v[60:63], v32 offset0:19 offset1:221
	v_pk_fma_f16 v2, v100, v6, v2
	v_pk_fma_f16 v3, v101, v7, v3
	v_pk_fma_f16 v4, v102, v8, v4
	v_pk_fma_f16 v5, v103, v9, v5
	v_cndmask_b32_e64 v26, v26, v18, s[66:67]
	s_waitcnt lgkmcnt(7)
	v_pk_fma_f16 v6, v2, v148, v149 op_sel:[0,0,0] op_sel_hi:[1,0,0] neg_lo:[1,0,0] neg_hi:[1,0,0]
	v_pk_fma_f16 v7, v3, v148, v149 op_sel:[0,0,0] op_sel_hi:[1,0,0] neg_lo:[1,0,0] neg_hi:[1,0,0]
	v_pk_fma_f16 v8, v4, v148, v149 op_sel:[0,0,0] op_sel_hi:[1,0,0] neg_lo:[1,0,0] neg_hi:[1,0,0]
	v_pk_fma_f16 v9, v5, v148, v149 op_sel:[0,0,0] op_sel_hi:[1,0,0] neg_lo:[1,0,0] neg_hi:[1,0,0]
	v_mfma_f32_16x16x32_f16 v[18:21], v[10:13], v[2:5], 0
	ds_read2_b64 v[64:67], v32 offset0:20 offset1:222
	ds_read_b128 v[128:131], v33 offset:160
	v_pk_fma_f16 v2, v104, v6, v2
	v_pk_fma_f16 v3, v105, v7, v3
	v_pk_fma_f16 v4, v106, v8, v4
	v_pk_fma_f16 v5, v107, v9, v5
	v_cndmask_b32_e64 v27, v27, v23, s[66:67]
	v_pk_fma_f16 v6, v2, v150, v151 op_sel:[0,0,0] op_sel_hi:[1,0,0] neg_lo:[1,0,0] neg_hi:[1,0,0]
	v_pk_fma_f16 v7, v3, v150, v151 op_sel:[0,0,0] op_sel_hi:[1,0,0] neg_lo:[1,0,0] neg_hi:[1,0,0]
	v_pk_fma_f16 v8, v4, v150, v151 op_sel:[0,0,0] op_sel_hi:[1,0,0] neg_lo:[1,0,0] neg_hi:[1,0,0]
	v_pk_fma_f16 v9, v5, v150, v151 op_sel:[0,0,0] op_sel_hi:[1,0,0] neg_lo:[1,0,0] neg_hi:[1,0,0]
	v_mfma_f32_16x16x32_f16 v[22:25], v[10:13], v[2:5], 0
	ds_read2_b64 v[68:71], v32 offset0:21 offset1:223
	v_pk_fma_f16 v2, v108, v6, v2
	v_pk_fma_f16 v3, v109, v7, v3
	v_pk_fma_f16 v4, v110, v8, v4
	v_pk_fma_f16 v5, v111, v9, v5
	v_cndmask_b32_e64 v28, v28, v20, s[66:67]
	s_waitcnt lgkmcnt(6)
	v_pk_fma_f16 v6, v2, v120, v121 op_sel:[0,0,0] op_sel_hi:[1,0,0] neg_lo:[1,0,0] neg_hi:[1,0,0]
	v_pk_fma_f16 v7, v3, v120, v121 op_sel:[0,0,0] op_sel_hi:[1,0,0] neg_lo:[1,0,0] neg_hi:[1,0,0]
	v_pk_fma_f16 v8, v4, v120, v121 op_sel:[0,0,0] op_sel_hi:[1,0,0] neg_lo:[1,0,0] neg_hi:[1,0,0]
	v_pk_fma_f16 v9, v5, v120, v121 op_sel:[0,0,0] op_sel_hi:[1,0,0] neg_lo:[1,0,0] neg_hi:[1,0,0]
	v_mfma_f32_16x16x32_f16 v[18:21], v[14:17], v[2:5], 0
	ds_read2_b64 v[72:75], v32 offset0:22 offset1:224
	ds_read_b128 v[132:135], v33 offset:176
	ds_read_b32 v37, v36 offset:8
	ds_read_b32 v38, v36 offset:72
	v_pk_fma_f16 v2, v48, v6, v2
	v_pk_fma_f16 v3, v49, v7, v3
	v_pk_fma_f16 v4, v50, v8, v4
	v_pk_fma_f16 v5, v51, v9, v5
	v_cndmask_b32_e64 v29, v29, v25, s[66:67]
	v_cvt_pk_f16_f32 v30, v26, v27
	v_cvt_pk_f16_f32 v31, v28, v29
	global_store_short v35, v30, s[68:69]
	global_store_short_d16_hi v35, v30, s[68:69] offset:64
	global_store_short v35, v31, s[68:69] offset:128
	global_store_short_d16_hi v35, v31, s[68:69] offset:192
	v_add_u32_e32 v35, 0x400, v35
	v_pk_fma_f16 v6, v2, v122, v123 op_sel:[0,0,0] op_sel_hi:[1,0,0] neg_lo:[1,0,0] neg_hi:[1,0,0]
	v_pk_fma_f16 v7, v3, v122, v123 op_sel:[0,0,0] op_sel_hi:[1,0,0] neg_lo:[1,0,0] neg_hi:[1,0,0]
	v_pk_fma_f16 v8, v4, v122, v123 op_sel:[0,0,0] op_sel_hi:[1,0,0] neg_lo:[1,0,0] neg_hi:[1,0,0]
	v_pk_fma_f16 v9, v5, v122, v123 op_sel:[0,0,0] op_sel_hi:[1,0,0] neg_lo:[1,0,0] neg_hi:[1,0,0]
	v_mfma_f32_16x16x32_f16 v[22:25], v[14:17], v[2:5], 0
	ds_read2_b64 v[76:79], v32 offset0:23 offset1:225
	v_pk_fma_f16 v2, v52, v6, v2
	v_pk_fma_f16 v3, v53, v7, v3
	v_pk_fma_f16 v4, v54, v8, v4
	v_pk_fma_f16 v5, v55, v9, v5
	v_cndmask_b32_e64 v26, v26, v18, s[60:61]
	s_waitcnt lgkmcnt(8)
	v_pk_fma_f16 v6, v2, v124, v125 op_sel:[0,0,0] op_sel_hi:[1,0,0] neg_lo:[1,0,0] neg_hi:[1,0,0]
	v_pk_fma_f16 v7, v3, v124, v125 op_sel:[0,0,0] op_sel_hi:[1,0,0] neg_lo:[1,0,0] neg_hi:[1,0,0]
	v_pk_fma_f16 v8, v4, v124, v125 op_sel:[0,0,0] op_sel_hi:[1,0,0] neg_lo:[1,0,0] neg_hi:[1,0,0]
	v_pk_fma_f16 v9, v5, v124, v125 op_sel:[0,0,0] op_sel_hi:[1,0,0] neg_lo:[1,0,0] neg_hi:[1,0,0]
	v_mfma_f32_16x16x32_f16 v[18:21], v[14:17], v[2:5], 0
	ds_read2_b64 v[80:83], v32 offset0:24 offset1:226
	ds_read_b128 v[136:139], v33 offset:192
	v_pk_fma_f16 v2, v56, v6, v2
	v_pk_fma_f16 v3, v57, v7, v3
	v_pk_fma_f16 v4, v58, v8, v4
	v_pk_fma_f16 v5, v59, v9, v5
	v_cndmask_b32_e64 v27, v27, v23, s[60:61]
	v_pk_fma_f16 v6, v2, v126, v127 op_sel:[0,0,0] op_sel_hi:[1,0,0] neg_lo:[1,0,0] neg_hi:[1,0,0]
	v_pk_fma_f16 v7, v3, v126, v127 op_sel:[0,0,0] op_sel_hi:[1,0,0] neg_lo:[1,0,0] neg_hi:[1,0,0]
	v_pk_fma_f16 v8, v4, v126, v127 op_sel:[0,0,0] op_sel_hi:[1,0,0] neg_lo:[1,0,0] neg_hi:[1,0,0]
	v_pk_fma_f16 v9, v5, v126, v127 op_sel:[0,0,0] op_sel_hi:[1,0,0] neg_lo:[1,0,0] neg_hi:[1,0,0]
	v_mfma_f32_16x16x32_f16 v[22:25], v[14:17], v[2:5], 0
	ds_read2_b64 v[84:87], v32 offset0:25 offset1:227
	v_pk_fma_f16 v2, v60, v6, v2
	v_pk_fma_f16 v3, v61, v7, v3
	v_pk_fma_f16 v4, v62, v8, v4
	v_pk_fma_f16 v5, v63, v9, v5
	v_cndmask_b32_e64 v28, v28, v20, s[60:61]
	s_waitcnt lgkmcnt(8)
	v_pk_fma_f16 v6, v2, v128, v129 op_sel:[0,0,0] op_sel_hi:[1,0,0] neg_lo:[1,0,0] neg_hi:[1,0,0]
	v_pk_fma_f16 v7, v3, v128, v129 op_sel:[0,0,0] op_sel_hi:[1,0,0] neg_lo:[1,0,0] neg_hi:[1,0,0]
	v_pk_fma_f16 v8, v4, v128, v129 op_sel:[0,0,0] op_sel_hi:[1,0,0] neg_lo:[1,0,0] neg_hi:[1,0,0]
	v_pk_fma_f16 v9, v5, v128, v129 op_sel:[0,0,0] op_sel_hi:[1,0,0] neg_lo:[1,0,0] neg_hi:[1,0,0]
	v_mfma_f32_16x16x32_f16 v[18:21], v[14:17], v[2:5], 0
	ds_read2_b64 v[88:91], v32 offset0:26 offset1:228
	ds_read_b128 v[140:143], v33 offset:208
	v_pk_fma_f16 v2, v64, v6, v2
	v_pk_fma_f16 v3, v65, v7, v3
	v_pk_fma_f16 v4, v66, v8, v4
	v_pk_fma_f16 v5, v67, v9, v5
	v_cndmask_b32_e64 v29, v29, v25, s[60:61]
	v_pk_fma_f16 v6, v2, v130, v131 op_sel:[0,0,0] op_sel_hi:[1,0,0] neg_lo:[1,0,0] neg_hi:[1,0,0]
	v_pk_fma_f16 v7, v3, v130, v131 op_sel:[0,0,0] op_sel_hi:[1,0,0] neg_lo:[1,0,0] neg_hi:[1,0,0]
	v_pk_fma_f16 v8, v4, v130, v131 op_sel:[0,0,0] op_sel_hi:[1,0,0] neg_lo:[1,0,0] neg_hi:[1,0,0]
	v_pk_fma_f16 v9, v5, v130, v131 op_sel:[0,0,0] op_sel_hi:[1,0,0] neg_lo:[1,0,0] neg_hi:[1,0,0]
	v_mfma_f32_16x16x32_f16 v[22:25], v[14:17], v[2:5], 0
	ds_read2_b64 v[92:95], v32 offset0:27 offset1:229
	v_pk_fma_f16 v2, v68, v6, v2
	v_pk_fma_f16 v3, v69, v7, v3
	v_pk_fma_f16 v4, v70, v8, v4
	v_pk_fma_f16 v5, v71, v9, v5
	v_cndmask_b32_e64 v26, v26, v18, s[62:63]
	s_waitcnt lgkmcnt(6)
	v_pk_fma_f16 v6, v2, v132, v133 op_sel:[0,0,0] op_sel_hi:[1,0,0] neg_lo:[1,0,0] neg_hi:[1,0,0]
	v_pk_fma_f16 v7, v3, v132, v133 op_sel:[0,0,0] op_sel_hi:[1,0,0] neg_lo:[1,0,0] neg_hi:[1,0,0]
	v_pk_fma_f16 v8, v4, v132, v133 op_sel:[0,0,0] op_sel_hi:[1,0,0] neg_lo:[1,0,0] neg_hi:[1,0,0]
	v_pk_fma_f16 v9, v5, v132, v133 op_sel:[0,0,0] op_sel_hi:[1,0,0] neg_lo:[1,0,0] neg_hi:[1,0,0]
	v_mfma_f32_16x16x32_f16 v[18:21], v[14:17], v[2:5], 0
	ds_read2_b64 v[96:99], v32 offset0:28 offset1:230
	ds_read_b128 v[144:147], v33 offset:224
	v_pk_fma_f16 v2, v72, v6, v2
	v_pk_fma_f16 v3, v73, v7, v3
	v_pk_fma_f16 v4, v74, v8, v4
	v_pk_fma_f16 v5, v75, v9, v5
	v_cndmask_b32_e64 v27, v27, v23, s[62:63]
	v_pk_fma_f16 v6, v2, v134, v135 op_sel:[0,0,0] op_sel_hi:[1,0,0] neg_lo:[1,0,0] neg_hi:[1,0,0]
	v_pk_fma_f16 v7, v3, v134, v135 op_sel:[0,0,0] op_sel_hi:[1,0,0] neg_lo:[1,0,0] neg_hi:[1,0,0]
	v_pk_fma_f16 v8, v4, v134, v135 op_sel:[0,0,0] op_sel_hi:[1,0,0] neg_lo:[1,0,0] neg_hi:[1,0,0]
	v_pk_fma_f16 v9, v5, v134, v135 op_sel:[0,0,0] op_sel_hi:[1,0,0] neg_lo:[1,0,0] neg_hi:[1,0,0]
	v_mfma_f32_16x16x32_f16 v[22:25], v[14:17], v[2:5], 0
	ds_read2_b64 v[100:103], v32 offset0:29 offset1:231
	v_pk_fma_f16 v2, v76, v6, v2
	v_pk_fma_f16 v3, v77, v7, v3
	v_pk_fma_f16 v4, v78, v8, v4
	v_pk_fma_f16 v5, v79, v9, v5
	v_cndmask_b32_e64 v28, v28, v20, s[62:63]
	s_waitcnt lgkmcnt(6)
	v_pk_fma_f16 v6, v2, v136, v137 op_sel:[0,0,0] op_sel_hi:[1,0,0] neg_lo:[1,0,0] neg_hi:[1,0,0]
	v_pk_fma_f16 v7, v3, v136, v137 op_sel:[0,0,0] op_sel_hi:[1,0,0] neg_lo:[1,0,0] neg_hi:[1,0,0]
	v_pk_fma_f16 v8, v4, v136, v137 op_sel:[0,0,0] op_sel_hi:[1,0,0] neg_lo:[1,0,0] neg_hi:[1,0,0]
	v_pk_fma_f16 v9, v5, v136, v137 op_sel:[0,0,0] op_sel_hi:[1,0,0] neg_lo:[1,0,0] neg_hi:[1,0,0]
	v_mfma_f32_16x16x32_f16 v[18:21], v[14:17], v[2:5], 0
	ds_read2_b64 v[104:107], v32 offset0:30 offset1:232
	ds_read_b128 v[148:151], v33 offset:240
	v_pk_fma_f16 v2, v80, v6, v2
	v_pk_fma_f16 v3, v81, v7, v3
	v_pk_fma_f16 v4, v82, v8, v4
	v_pk_fma_f16 v5, v83, v9, v5
	v_cndmask_b32_e64 v29, v29, v25, s[62:63]
	v_readfirstlane_b32 s4, v37
	v_readfirstlane_b32 s5, v38
	s_and_b32 s4, s4, s5
	s_cbranch_scc0 .Lc0_slow1
.Lc0_back1:
	v_pk_fma_f16 v6, v2, v138, v139 op_sel:[0,0,0] op_sel_hi:[1,0,0] neg_lo:[1,0,0] neg_hi:[1,0,0]
	v_pk_fma_f16 v7, v3, v138, v139 op_sel:[0,0,0] op_sel_hi:[1,0,0] neg_lo:[1,0,0] neg_hi:[1,0,0]
	v_pk_fma_f16 v8, v4, v138, v139 op_sel:[0,0,0] op_sel_hi:[1,0,0] neg_lo:[1,0,0] neg_hi:[1,0,0]
	v_pk_fma_f16 v9, v5, v138, v139 op_sel:[0,0,0] op_sel_hi:[1,0,0] neg_lo:[1,0,0] neg_hi:[1,0,0]
	v_mfma_f32_16x16x32_f16 v[22:25], v[14:17], v[2:5], 0
	ds_read2_b64 v[108:111], v32 offset0:31 offset1:233
	v_pk_fma_f16 v2, v84, v6, v2
	v_pk_fma_f16 v3, v85, v7, v3
	v_pk_fma_f16 v4, v86, v8, v4
	v_pk_fma_f16 v5, v87, v9, v5
	v_cndmask_b32_e64 v26, v26, v18, s[64:65]
	s_waitcnt lgkmcnt(6)
	v_pk_fma_f16 v6, v2, v140, v141 op_sel:[0,0,0] op_sel_hi:[1,0,0] neg_lo:[1,0,0] neg_hi:[1,0,0]
	v_pk_fma_f16 v7, v3, v140, v141 op_sel:[0,0,0] op_sel_hi:[1,0,0] neg_lo:[1,0,0] neg_hi:[1,0,0]
	v_pk_fma_f16 v8, v4, v140, v141 op_sel:[0,0,0] op_sel_hi:[1,0,0] neg_lo:[1,0,0] neg_hi:[1,0,0]
	v_pk_fma_f16 v9, v5, v140, v141 op_sel:[0,0,0] op_sel_hi:[1,0,0] neg_lo:[1,0,0] neg_hi:[1,0,0]
	v_mfma_f32_16x16x32_f16 v[18:21], v[14:17], v[2:5], 0
	ds_read2_b64 v[48:51], v32 offset0:32 offset1:234
	ds_read_b128 v[120:123], v33 offset:256
	ds_read2_b64 v[10:13], v34 offset0:32 offset1:234
	v_pk_fma_f16 v2, v88, v6, v2
	v_pk_fma_f16 v3, v89, v7, v3
	v_pk_fma_f16 v4, v90, v8, v4
	v_pk_fma_f16 v5, v91, v9, v5
	v_cndmask_b32_e64 v27, v27, v23, s[64:65]
	v_pk_fma_f16 v6, v2, v142, v143 op_sel:[0,0,0] op_sel_hi:[1,0,0] neg_lo:[1,0,0] neg_hi:[1,0,0]
	v_pk_fma_f16 v7, v3, v142, v143 op_sel:[0,0,0] op_sel_hi:[1,0,0] neg_lo:[1,0,0] neg_hi:[1,0,0]
	v_pk_fma_f16 v8, v4, v142, v143 op_sel:[0,0,0] op_sel_hi:[1,0,0] neg_lo:[1,0,0] neg_hi:[1,0,0]
	v_pk_fma_f16 v9, v5, v142, v143 op_sel:[0,0,0] op_sel_hi:[1,0,0] neg_lo:[1,0,0] neg_hi:[1,0,0]
	v_mfma_f32_16x16x32_f16 v[22:25], v[14:17], v[2:5], 0
	ds_read2_b64 v[52:55], v32 offset0:33 offset1:235
	v_pk_fma_f16 v2, v92, v6, v2
	v_pk_fma_f16 v3, v93, v7, v3
	v_pk_fma_f16 v4, v94, v8, v4
	v_pk_fma_f16 v5, v95, v9, v5
	v_cndmask_b32_e64 v28, v28, v20, s[64:65]
	s_waitcnt lgkmcnt(7)
	v_pk_fma_f16 v6, v2, v144, v145 op_sel:[0,0,0] op_sel_hi:[1,0,0] neg_lo:[1,0,0] neg_hi:[1,0,0]
	v_pk_fma_f16 v7, v3, v144, v145 op_sel:[0,0,0] op_sel_hi:[1,0,0] neg_lo:[1,0,0] neg_hi:[1,0,0]
	v_pk_fma_f16 v8, v4, v144, v145 op_sel:[0,0,0] op_sel_hi:[1,0,0] neg_lo:[1,0,0] neg_hi:[1,0,0]
	v_pk_fma_f16 v9, v5, v144, v145 op_sel:[0,0,0] op_sel_hi:[1,0,0] neg_lo:[1,0,0] neg_hi:[1,0,0]
	v_mfma_f32_16x16x32_f16 v[18:21], v[14:17], v[2:5], 0
	ds_read2_b64 v[56:59], v32 offset0:34 offset1:236
	ds_read_b128 v[124:127], v33 offset:272
	v_pk_fma_f16 v2, v96, v6, v2
	v_pk_fma_f16 v3, v97, v7, v3
	v_pk_fma_f16 v4, v98, v8, v4
	v_pk_fma_f16 v5, v99, v9, v5
	v_cndmask_b32_e64 v29, v29, v25, s[64:65]
	v_pk_fma_f16 v6, v2, v146, v147 op_sel:[0,0,0] op_sel_hi:[1,0,0] neg_lo:[1,0,0] neg_hi:[1,0,0]
	v_pk_fma_f16 v7, v3, v146, v147 op_sel:[0,0,0] op_sel_hi:[1,0,0] neg_lo:[1,0,0] neg_hi:[1,0,0]
	v_pk_fma_f16 v8, v4, v146, v147 op_sel:[0,0,0] op_sel_hi:[1,0,0] neg_lo:[1,0,0] neg_hi:[1,0,0]
	v_pk_fma_f16 v9, v5, v146, v147 op_sel:[0,0,0] op_sel_hi:[1,0,0] neg_lo:[1,0,0] neg_hi:[1,0,0]
	v_mfma_f32_16x16x32_f16 v[22:25], v[14:17], v[2:5], 0
	ds_read2_b64 v[60:63], v32 offset0:35 offset1:237
	v_pk_fma_f16 v2, v100, v6, v2
	v_pk_fma_f16 v3, v101, v7, v3
	v_pk_fma_f16 v4, v102, v8, v4
	v_pk_fma_f16 v5, v103, v9, v5
	v_cndmask_b32_e64 v26, v26, v18, s[66:67]
	s_waitcnt lgkmcnt(7)
	v_pk_fma_f16 v6, v2, v148, v149 op_sel:[0,0,0] op_sel_hi:[1,0,0] neg_lo:[1,0,0] neg_hi:[1,0,0]
	v_pk_fma_f16 v7, v3, v148, v149 op_sel:[0,0,0] op_sel_hi:[1,0,0] neg_lo:[1,0,0] neg_hi:[1,0,0]
	v_pk_fma_f16 v8, v4, v148, v149 op_sel:[0,0,0] op_sel_hi:[1,0,0] neg_lo:[1,0,0] neg_hi:[1,0,0]
	v_pk_fma_f16 v9, v5, v148, v149 op_sel:[0,0,0] op_sel_hi:[1,0,0] neg_lo:[1,0,0] neg_hi:[1,0,0]
	v_mfma_f32_16x16x32_f16 v[18:21], v[14:17], v[2:5], 0
	ds_read2_b64 v[64:67], v32 offset0:36 offset1:238
	ds_read_b128 v[128:131], v33 offset:288
	v_pk_fma_f16 v2, v104, v6, v2
	v_pk_fma_f16 v3, v105, v7, v3
	v_pk_fma_f16 v4, v106, v8, v4
	v_pk_fma_f16 v5, v107, v9, v5
	v_cndmask_b32_e64 v27, v27, v23, s[66:67]
	v_pk_fma_f16 v6, v2, v150, v151 op_sel:[0,0,0] op_sel_hi:[1,0,0] neg_lo:[1,0,0] neg_hi:[1,0,0]
	v_pk_fma_f16 v7, v3, v150, v151 op_sel:[0,0,0] op_sel_hi:[1,0,0] neg_lo:[1,0,0] neg_hi:[1,0,0]
	v_pk_fma_f16 v8, v4, v150, v151 op_sel:[0,0,0] op_sel_hi:[1,0,0] neg_lo:[1,0,0] neg_hi:[1,0,0]
	v_pk_fma_f16 v9, v5, v150, v151 op_sel:[0,0,0] op_sel_hi:[1,0,0] neg_lo:[1,0,0] neg_hi:[1,0,0]
	v_mfma_f32_16x16x32_f16 v[22:25], v[14:17], v[2:5], 0
	ds_read2_b64 v[68:71], v32 offset0:37 offset1:239
	v_pk_fma_f16 v2, v108, v6, v2
	v_pk_fma_f16 v3, v109, v7, v3
	v_pk_fma_f16 v4, v110, v8, v4
	v_pk_fma_f16 v5, v111, v9, v5
	v_cndmask_b32_e64 v28, v28, v20, s[66:67]
	v_add_u32_e32 v32, 0x100, v32
	v_add_u32_e32 v33, 0x100, v33
	v_add_u32_e32 v34, 0x100, v34
	v_add_u32_e32 v36, 8, v36
	s_add_i32 s70, s70, 1
	s_cmp_lt_u32 s70, 6
	s_cbranch_scc1 .Lc0_loop
	s_waitcnt lgkmcnt(6)
	v_pk_fma_f16 v6, v2, v120, v121 op_sel:[0,0,0] op_sel_hi:[1,0,0] neg_lo:[1,0,0] neg_hi:[1,0,0]
	v_pk_fma_f16 v7, v3, v120, v121 op_sel:[0,0,0] op_sel_hi:[1,0,0] neg_lo:[1,0,0] neg_hi:[1,0,0]
	v_pk_fma_f16 v8, v4, v120, v121 op_sel:[0,0,0] op_sel_hi:[1,0,0] neg_lo:[1,0,0] neg_hi:[1,0,0]
	v_pk_fma_f16 v9, v5, v120, v121 op_sel:[0,0,0] op_sel_hi:[1,0,0] neg_lo:[1,0,0] neg_hi:[1,0,0]
	v_mfma_f32_16x16x32_f16 v[18:21], v[10:13], v[2:5], 0
	ds_read2_b64 v[72:75], v32 offset0:6 offset1:208
	ds_read_b128 v[132:135], v33 offset:48
	v_pk_fma_f16 v2, v48, v6, v2
	v_pk_fma_f16 v3, v49, v7, v3
	v_pk_fma_f16 v4, v50, v8, v4
	v_pk_fma_f16 v5, v51, v9, v5
	v_cndmask_b32_e64 v29, v29, v25, s[66:67]
	v_cvt_pk_f16_f32 v30, v26, v27
	v_cvt_pk_f16_f32 v31, v28, v29
	global_store_short v35, v30, s[68:69]
	global_store_short_d16_hi v35, v30, s[68:69] offset:64
	global_store_short v35, v31, s[68:69] offset:128
	global_store_short_d16_hi v35, v31, s[68:69] offset:192
	v_add_u32_e32 v35, 0x400, v35
	v_pk_fma_f16 v6, v2, v122, v123 op_sel:[0,0,0] op_sel_hi:[1,0,0] neg_lo:[1,0,0] neg_hi:[1,0,0]
	v_pk_fma_f16 v7, v3, v122, v123 op_sel:[0,0,0] op_sel_hi:[1,0,0] neg_lo:[1,0,0] neg_hi:[1,0,0]
	v_pk_fma_f16 v8, v4, v122, v123 op_sel:[0,0,0] op_sel_hi:[1,0,0] neg_lo:[1,0,0] neg_hi:[1,0,0]
	v_pk_fma_f16 v9, v5, v122, v123 op_sel:[0,0,0] op_sel_hi:[1,0,0] neg_lo:[1,0,0] neg_hi:[1,0,0]
	v_mfma_f32_16x16x32_f16 v[22:25], v[10:13], v[2:5], 0
	ds_read2_b64 v[76:79], v32 offset0:7 offset1:209
	v_pk_fma_f16 v2, v52, v6, v2
	v_pk_fma_f16 v3, v53, v7, v3
	v_pk_fma_f16 v4, v54, v8, v4
	v_pk_fma_f16 v5, v55, v9, v5
	v_cndmask_b32_e64 v26, v26, v18, s[60:61]
	s_waitcnt lgkmcnt(6)
	v_pk_fma_f16 v6, v2, v124, v125 op_sel:[0,0,0] op_sel_hi:[1,0,0] neg_lo:[1,0,0] neg_hi:[1,0,0]
	v_pk_fma_f16 v7, v3, v124, v125 op_sel:[0,0,0] op_sel_hi:[1,0,0] neg_lo:[1,0,0] neg_hi:[1,0,0]
	v_pk_fma_f16 v8, v4, v124, v125 op_sel:[0,0,0] op_sel_hi:[1,0,0] neg_lo:[1,0,0] neg_hi:[1,0,0]
	v_pk_fma_f16 v9, v5, v124, v125 op_sel:[0,0,0] op_sel_hi:[1,0,0] neg_lo:[1,0,0] neg_hi:[1,0,0]
	v_mfma_f32_16x16x32_f16 v[18:21], v[10:13], v[2:5], 0
	v_pk_fma_f16 v2, v56, v6, v2
	v_pk_fma_f16 v3, v57, v7, v3
	v_pk_fma_f16 v4, v58, v8, v4
	v_pk_fma_f16 v5, v59, v9, v5
	v_cndmask_b32_e64 v27, v27, v23, s[60:61]
	v_pk_fma_f16 v6, v2, v126, v127 op_sel:[0,0,0] op_sel_hi:[1,0,0] neg_lo:[1,0,0] neg_hi:[1,0,0]
	v_pk_fma_f16 v7, v3, v126, v127 op_sel:[0,0,0] op_sel_hi:[1,0,0] neg_lo:[1,0,0] neg_hi:[1,0,0]
	v_pk_fma_f16 v8, v4, v126, v127 op_sel:[0,0,0] op_sel_hi:[1,0,0] neg_lo:[1,0,0] neg_hi:[1,0,0]
	v_pk_fma_f16 v9, v5, v126, v127 op_sel:[0,0,0] op_sel_hi:[1,0,0] neg_lo:[1,0,0] neg_hi:[1,0,0]
	v_mfma_f32_16x16x32_f16 v[22:25], v[10:13], v[2:5], 0
	v_pk_fma_f16 v2, v60, v6, v2
	v_pk_fma_f16 v3, v61, v7, v3
	v_pk_fma_f16 v4, v62, v8, v4
	v_pk_fma_f16 v5, v63, v9, v5
	v_cndmask_b32_e64 v28, v28, v20, s[60:61]
	s_waitcnt lgkmcnt(3)
	v_pk_fma_f16 v6, v2, v128, v129 op_sel:[0,0,0] op_sel_hi:[1,0,0] neg_lo:[1,0,0] neg_hi:[1,0,0]
	v_pk_fma_f16 v7, v3, v128, v129 op_sel:[0,0,0] op_sel_hi:[1,0,0] neg_lo:[1,0,0] neg_hi:[1,0,0]
	v_pk_fma_f16 v8, v4, v128, v129 op_sel:[0,0,0] op_sel_hi:[1,0,0] neg_lo:[1,0,0] neg_hi:[1,0,0]
	v_pk_fma_f16 v9, v5, v128, v129 op_sel:[0,0,0] op_sel_hi:[1,0,0] neg_lo:[1,0,0] neg_hi:[1,0,0]
	v_mfma_f32_16x16x32_f16 v[18:21], v[10:13], v[2:5], 0
	v_pk_fma_f16 v2, v64, v6, v2
	v_pk_fma_f16 v3, v65, v7, v3
	v_pk_fma_f16 v4, v66, v8, v4
	v_pk_fma_f16 v5, v67, v9, v5
	v_cndmask_b32_e64 v29, v29, v25, s[60:61]
	v_pk_fma_f16 v6, v2, v130, v131 op_sel:[0,0,0] op_sel_hi:[1,0,0] neg_lo:[1,0,0] neg_hi:[1,0,0]
	v_pk_fma_f16 v7, v3, v130, v131 op_sel:[0,0,0] op_sel_hi:[1,0,0] neg_lo:[1,0,0] neg_hi:[1,0,0]
	v_pk_fma_f16 v8, v4, v130, v131 op_sel:[0,0,0] op_sel_hi:[1,0,0] neg_lo:[1,0,0] neg_hi:[1,0,0]
	v_pk_fma_f16 v9, v5, v130, v131 op_sel:[0,0,0] op_sel_hi:[1,0,0] neg_lo:[1,0,0] neg_hi:[1,0,0]
	v_mfma_f32_16x16x32_f16 v[22:25], v[10:13], v[2:5], 0
	v_pk_fma_f16 v2, v68, v6, v2
	v_pk_fma_f16 v3, v69, v7, v3
	v_pk_fma_f16 v4, v70, v8, v4
	v_pk_fma_f16 v5, v71, v9, v5
	v_cndmask_b32_e64 v26, v26, v18, s[62:63]
	s_waitcnt lgkmcnt(0)
	v_pk_fma_f16 v6, v2, v132, v133 op_sel:[0,0,0] op_sel_hi:[1,0,0] neg_lo:[1,0,0] neg_hi:[1,0,0]
	v_pk_fma_f16 v7, v3, v132, v133 op_sel:[0,0,0] op_sel_hi:[1,0,0] neg_lo:[1,0,0] neg_hi:[1,0,0]
	v_pk_fma_f16 v8, v4, v132, v133 op_sel:[0,0,0] op_sel_hi:[1,0,0] neg_lo:[1,0,0] neg_hi:[1,0,0]
	v_pk_fma_f16 v9, v5, v132, v133 op_sel:[0,0,0] op_sel_hi:[1,0,0] neg_lo:[1,0,0] neg_hi:[1,0,0]
	v_mfma_f32_16x16x32_f16 v[18:21], v[10:13], v[2:5], 0
	v_pk_fma_f16 v2, v72, v6, v2
	v_pk_fma_f16 v3, v73, v7, v3
	v_pk_fma_f16 v4, v74, v8, v4
	v_pk_fma_f16 v5, v75, v9, v5
	v_cndmask_b32_e64 v27, v27, v23, s[62:63]
	v_pk_fma_f16 v6, v2, v134, v135 op_sel:[0,0,0] op_sel_hi:[1,0,0] neg_lo:[1,0,0] neg_hi:[1,0,0]
	v_pk_fma_f16 v7, v3, v134, v135 op_sel:[0,0,0] op_sel_hi:[1,0,0] neg_lo:[1,0,0] neg_hi:[1,0,0]
	v_pk_fma_f16 v8, v4, v134, v135 op_sel:[0,0,0] op_sel_hi:[1,0,0] neg_lo:[1,0,0] neg_hi:[1,0,0]
	v_pk_fma_f16 v9, v5, v134, v135 op_sel:[0,0,0] op_sel_hi:[1,0,0] neg_lo:[1,0,0] neg_hi:[1,0,0]
	v_mfma_f32_16x16x32_f16 v[22:25], v[10:13], v[2:5], 0
	v_pk_fma_f16 v2, v76, v6, v2
	v_pk_fma_f16 v3, v77, v7, v3
	v_pk_fma_f16 v4, v78, v8, v4
	v_pk_fma_f16 v5, v79, v9, v5
	v_cndmask_b32_e64 v28, v28, v20, s[62:63]
	s_nop 7
	v_cndmask_b32_e64 v29, v29, v25, s[62:63]
	v_cvt_pk_f16_f32 v30, v26, v27
	v_cvt_pk_f16_f32 v31, v28, v29
	s_mov_b32 exec_lo, -1
	s_mov_b32 exec_hi, 0
	global_store_short v35, v30, s[68:69]
	global_store_short_d16_hi v35, v30, s[68:69] offset:64
	global_store_short v35, v31, s[68:69] offset:128
	global_store_short_d16_hi v35, v31, s[68:69] offset:192
	s_endpgm
.Lc0_slow0:
	s_sleep 1
	ds_read_b32 v37, v36 offset:4
	ds_read_b32 v38, v36 offset:68
	s_waitcnt lgkmcnt(0)
	v_readfirstlane_b32 s4, v37
	v_readfirstlane_b32 s5, v38
	s_and_b32 s4, s4, s5
	s_cbranch_scc0 .Lc0_slow0
	s_branch .Lc0_back0
.Lc0_slow1:
	s_sleep 1
	ds_read_b32 v37, v36 offset:8
	ds_read_b32 v38, v36 offset:72
	s_waitcnt lgkmcnt(0)
	v_readfirstlane_b32 s4, v37
	v_readfirstlane_b32 s5, v38
	s_and_b32 s4, s4, s5
	s_cbranch_scc0 .Lc0_slow1
	s_branch .Lc0_back1
.Lc_par1:
	ds_read2_b64 v[48:51], v32 offset0:0 offset1:202
	ds_read_b128 v[120:123], v33 offset:0
	ds_read2_b64 v[10:13], v34 offset0:0 offset1:202
	ds_read2_b64 v[52:55], v32 offset0:1 offset1:203
	ds_read2_b64 v[56:59], v32 offset0:2 offset1:204
	ds_read_b128 v[124:127], v33 offset:16
	ds_read2_b64 v[60:63], v32 offset0:3 offset1:205
	ds_read2_b64 v[64:67], v32 offset0:4 offset1:206
	ds_read_b128 v[128:131], v33 offset:32
	ds_read2_b64 v[68:71], v32 offset0:5 offset1:207
	s_mov_b32 s70, 0
.Lc1_loop:
	s_waitcnt lgkmcnt(6)
	v_pk_fma_f16 v6, v2, v120, v121 op_sel:[0,1,1] op_sel_hi:[1,1,1] neg_lo:[1,0,0] neg_hi:[1,0,0]
	v_pk_fma_f16 v7, v3, v120, v121 op_sel:[0,1,1] op_sel_hi:[1,1,1] neg_lo:[1,0,0] neg_hi:[1,0,0]
	v_pk_fma_f16 v8, v4, v120, v121 op_sel:[0,1,1] op_sel_hi:[1,1,1] neg_lo:[1,0,0] neg_hi:[1,0,0]
	v_pk_fma_f16 v9, v5, v120, v121 op_sel:[0,1,1] op_sel_hi:[1,1,1] neg_lo:[1,0,0] neg_hi:[1,0,0]
	v_mfma_f32_16x16x32_f16 v[18:21], v[10:13], v[2:5], 0
	ds_read2_b64 v[72:75], v32 offset0:6 offset1:208
	ds_read_b128 v[132:135], v33 offset:48
	ds_read_b32 v37, v36 offset:4
	ds_read_b32 v38, v36 offset:68
	v_pk_fma_f16 v2, v48, v6, v2
	v_pk_fma_f16 v3, v49, v7, v3
	v_pk_fma_f16 v4, v50, v8, v4
	v_pk_fma_f16 v5, v51, v9, v5
	v_cndmask_b32_e64 v29, v29, v25, s[66:67]
	s_cmp_eq_u32 s70, 0
	s_cbranch_scc1 .Lc1_nost
	v_cvt_pk_f16_f32 v30, v26, v27
	v_cvt_pk_f16_f32 v31, v28, v29
	global_store_short v35, v30, s[68:69]
	global_store_short_d16_hi v35, v30, s[68:69] offset:64
	global_store_short v35, v31, s[68:69] offset:128
	global_store_short_d16_hi v35, v31, s[68:69] offset:192
	v_add_u32_e32 v35, 0x400, v35
.Lc1_nost:
	v_pk_fma_f16 v6, v2, v122, v123 op_sel:[0,1,1] op_sel_hi:[1,1,1] neg_lo:[1,0,0] neg_hi:[1,0,0]
	v_pk_fma_f16 v7, v3, v122, v123 op_sel:[0,1,1] op_sel_hi:[1,1,1] neg_lo:[1,0,0] neg_hi:[1,0,0]
	v_pk_fma_f16 v8, v4, v122, v123 op_sel:[0,1,1] op_sel_hi:[1,1,1] neg_lo:[1,0,0] neg_hi:[1,0,0]
	v_pk_fma_f16 v9, v5, v122, v123 op_sel:[0,1,1] op_sel_hi:[1,1,1] neg_lo:[1,0,0] neg_hi:[1,0,0]
	v_mfma_f32_16x16x32_f16 v[22:25], v[10:13], v[2:5], 0
	ds_read2_b64 v[76:79], v32 offset0:7 offset1:209
	v_pk_fma_f16 v2, v52, v6, v2
	v_pk_fma_f16 v3, v53, v7, v3
	v_pk_fma_f16 v4, v54, v8, v4
	v_pk_fma_f16 v5, v55, v9, v5
	v_cndmask_b32_e64 v26, v26, v18, s[60:61]
	s_waitcnt lgkmcnt(8)
	v_pk_fma_f16 v6, v2, v124, v125 op_sel:[0,1,1] op_sel_hi:[1,1,1] neg_lo:[1,0,0] neg_hi:[1,0,0]
	v_pk_fma_f16 v7, v3, v124, v125 op_sel:[0,1,1] op_sel_hi:[1,1,1] neg_lo:[1,0,0] neg_hi:[1,0,0]
	v_pk_fma_f16 v8, v4, v124, v125 op_sel:[0,1,1] op_sel_hi:[1,1,1] neg_lo:[1,0,0] neg_hi:[1,0,0]
	v_pk_fma_f16 v9, v5, v124, v125 op_sel:[0,1,1] op_sel_hi:[1,1,1] neg_lo:[1,0,0] neg_hi:[1,0,0]
	v_mfma_f32_16x16x32_f16 v[18:21], v[10:13], v[2:5], 0
	ds_read2_b64 v[80:83], v32 offset0:8 offset1:210
	ds_read_b128 v[136:139], v33 offset:64
	v_pk_fma_f16 v2, v56, v6, v2
	v_pk_fma_f16 v3, v57, v7, v3
	v_pk_fma_f16 v4, v58, v8, v4
	v_pk_fma_f16 v5, v59, v9, v5
	v_cndmask_b32_e64 v27, v27, v23, s[60:61]
	v_pk_fma_f16 v6, v2, v126, v127 op_sel:[0,1,1] op_sel_hi:[1,1,1] neg_lo:[1,0,0] neg_hi:[1,0,0]
	v_pk_fma_f16 v7, v3, v126, v127 op_sel:[0,1,1] op_sel_hi:[1,1,1] neg_lo:[1,0,0] neg_hi:[1,0,0]
	v_pk_fma_f16 v8, v4, v126, v127 op_sel:[0,1,1] op_sel_hi:[1,1,1] neg_lo:[1,0,0] neg_hi:[1,0,0]
	v_pk_fma_f16 v9, v5, v126, v127 op_sel:[0,1,1] op_sel_hi:[1,1,1] neg_lo:[1,0,0] neg_hi:[1,0,0]
	v_mfma_f32_16x16x32_f16 v[22:25], v[10:13], v[2:5], 0
	ds_read2_b64 v[84:87], v32 offset0:9 offset1:211
	v_pk_fma_f16 v2, v60, v6, v2
	v_pk_fma_f16 v3, v61, v7, v3
	v_pk_fma_f16 v4, v62, v8, v4
	v_pk_fma_f16 v5, v63, v9, v5
	v_cndmask_b32_e64 v28, v28, v20, s[60:61]
	s_waitcnt lgkmcnt(8)
	v_pk_fma_f16 v6, v2, v128, v129 op_sel:[0,1,1] op_sel_hi:[1,1,1] neg_lo:[1,0,0] neg_hi:[1,0,0]
	v_pk_fma_f16 v7, v3, v128, v129 op_sel:[0,1,1] op_sel_hi:[1,1,1] neg_lo:[1,0,0] neg_hi:[1,0,0]
	v_pk_fma_f16 v8, v4, v128, v129 op_sel:[0,1,1] op_sel_hi:[1,1,1] neg_lo:[1,0,0] neg_hi:[1,0,0]
	v_pk_fma_f16 v9, v5, v128, v129 op_sel:[0,1,1] op_sel_hi:[1,1,1] neg_lo:[1,0,0] neg_hi:[1,0,0]
	v_mfma_f32_16x16x32_f16 v[18:21], v[10:13], v[2:5], 0
	ds_read2_b64 v[88:91], v32 offset0:10 offset1:212
	ds_read_b128 v[140:143], v33 offset:80
	v_pk_fma_f16 v2, v64, v6, v2
	v_pk_fma_f16 v3, v65, v7, v3
	v_pk_fma_f16 v4, v66, v8, v4
	v_pk_fma_f16 v5, v67, v9, v5
	v_cndmask_b32_e64 v29, v29, v25, s[60:61]
	v_pk_fma_f16 v6, v2, v130, v131 op_sel:[0,1,1] op_sel_hi:[1,1,1] neg_lo:[1,0,0] neg_hi:[1,0,0]
	v_pk_fma_f16 v7, v3, v130, v131 op_sel:[0,1,1] op_sel_hi:[1,1,1] neg_lo:[1,0,0] neg_hi:[1,0,0]
	v_pk_fma_f16 v8, v4, v130, v131 op_sel:[0,1,1] op_sel_hi:[1,1,1] neg_lo:[1,0,0] neg_hi:[1,0,0]
	v_pk_fma_f16 v9, v5, v130, v131 op_sel:[0,1,1] op_sel_hi:[1,1,1] neg_lo:[1,0,0] neg_hi:[1,0,0]
	v_mfma_f32_16x16x32_f16 v[22:25], v[10:13], v[2:5], 0
	ds_read2_b64 v[92:95], v32 offset0:11 offset1:213
	v_pk_fma_f16 v2, v68, v6, v2
	v_pk_fma_f16 v3, v69, v7, v3
	v_pk_fma_f16 v4, v70, v8, v4
	v_pk_fma_f16 v5, v71, v9, v5
	v_cndmask_b32_e64 v26, v26, v18, s[62:63]
	s_waitcnt lgkmcnt(6)
	v_pk_fma_f16 v6, v2, v132, v133 op_sel:[0,1,1] op_sel_hi:[1,1,1] neg_lo:[1,0,0] neg_hi:[1,0,0]
	v_pk_fma_f16 v7, v3, v132, v133 op_sel:[0,1,1] op_sel_hi:[1,1,1] neg_lo:[1,0,0] neg_hi:[1,0,0]
	v_pk_fma_f16 v8, v4, v132, v133 op_sel:[0,1,1] op_sel_hi:[1,1,1] neg_lo:[1,0,0] neg_hi:[1,0,0]
	v_pk_fma_f16 v9, v5, v132, v133 op_sel:[0,1,1] op_sel_hi:[1,1,1] neg_lo:[1,0,0] neg_hi:[1,0,0]
	v_mfma_f32_16x16x32_f16 v[18:21], v[10:13], v[2:5], 0
	ds_read2_b64 v[96:99], v32 offset0:12 offset1:214
	ds_read_b128 v[144:147], v33 offset:96
	v_pk_fma_f16 v2, v72, v6, v2
	v_pk_fma_f16 v3, v73, v7, v3
	v_pk_fma_f16 v4, v74, v8, v4
	v_pk_fma_f16 v5, v75, v9, v5
	v_cndmask_b32_e64 v27, v27, v23, s[62:63]
	v_pk_fma_f16 v6, v2, v134, v135 op_sel:[0,1,1] op_sel_hi:[1,1,1] neg_lo:[1,0,0] neg_hi:[1,0,0]
	v_pk_fma_f16 v7, v3, v134, v135 op_sel:[0,1,1] op_sel_hi:[1,1,1] neg_lo:[1,0,0] neg_hi:[1,0,0]
	v_pk_fma_f16 v8, v4, v134, v135 op_sel:[0,1,1] op_sel_hi:[1,1,1] neg_lo:[1,0,0] neg_hi:[1,0,0]
	v_pk_fma_f16 v9, v5, v134, v135 op_sel:[0,1,1] op_sel_hi:[1,1,1] neg_lo:[1,0,0] neg_hi:[1,0,0]
	v_mfma_f32_16x16x32_f16 v[22:25], v[10:13], v[2:5], 0
	ds_read2_b64 v[100:103], v32 offset0:13 offset1:215
	v_pk_fma_f16 v2, v76, v6, v2
	v_pk_fma_f16 v3, v77, v7, v3
	v_pk_fma_f16 v4, v78, v8, v4
	v_pk_fma_f16 v5, v79, v9, v5
	v_cndmask_b32_e64 v28, v28, v20, s[62:63]
	s_waitcnt lgkmcnt(6)
	v_pk_fma_f16 v6, v2, v136, v137 op_sel:[0,1,1] op_sel_hi:[1,1,1] neg_lo:[1,0,0] neg_hi:[1,0,0]
	v_pk_fma_f16 v7, v3, v136, v137 op_sel:[0,1,1] op_sel_hi:[1,1,1] neg_lo:[1,0,0] neg_hi:[1,0,0]
	v_pk_fma_f16 v8, v4, v136, v137 op_sel:[0,1,1] op_sel_hi:[1,1,1] neg_lo:[1,0,0] neg_hi:[1,0,0]
	v_pk_fma_f16 v9, v5, v136, v137 op_sel:[0,1,1] op_sel_hi:[1,1,1] neg_lo:[1,0,0] neg_hi:[1,0,0]
	v_mfma_f32_16x16x32_f16 v[18:21], v[10:13], v[2:5], 0
	ds_read2_b64 v[104:107], v32 offset0:14 offset1:216
	ds_read_b128 v[148:151], v33 offset:112
	v_pk_fma_f16 v2, v80, v6, v2
	v_pk_fma_f16 v3, v81, v7, v3
	v_pk_fma_f16 v4, v82, v8, v4
	v_pk_fma_f16 v5, v83, v9, v5
	v_cndmask_b32_e64 v29, v29, v25, s[62:63]
	v_readfirstlane_b32 s4, v37
	v_readfirstlane_b32 s5, v38
	s_and_b32 s4, s4, s5
	s_cbranch_scc0 .Lc1_slow0
.Lc1_back0:
	v_pk_fma_f16 v6, v2, v138, v139 op_sel:[0,1,1] op_sel_hi:[1,1,1] neg_lo:[1,0,0] neg_hi:[1,0,0]
	v_pk_fma_f16 v7, v3, v138, v139 op_sel:[0,1,1] op_sel_hi:[1,1,1] neg_lo:[1,0,0] neg_hi:[1,0,0]
	v_pk_fma_f16 v8, v4, v138, v139 op_sel:[0,1,1] op_sel_hi:[1,1,1] neg_lo:[1,0,0] neg_hi:[1,0,0]
	v_pk_fma_f16 v9, v5, v138, v139 op_sel:[0,1,1] op_sel_hi:[1,1,1] neg_lo:[1,0,0] neg_hi:[1,0,0]
	v_mfma_f32_16x16x32_f16 v[22:25], v[10:13], v[2:5], 0
	ds_read2_b64 v[108:111], v32 offset0:15 offset1:217
	v_pk_fma_f16 v2, v84, v6, v2
	v_pk_fma_f16 v3, v85, v7, v3
	v_pk_fma_f16 v4, v86, v8, v4
	v_pk_fma_f16 v5, v87, v9, v5
	v_cndmask_b32_e64 v26, v26, v18, s[64:65]
	s_waitcnt lgkmcnt(6)
	v_pk_fma_f16 v6, v2, v140, v141 op_sel:[0,1,1] op_sel_hi:[1,1,1] neg_lo:[1,0,0] neg_hi:[1,0,0]
	v_pk_fma_f16 v7, v3, v140, v141 op_sel:[0,1,1] op_sel_hi:[1,1,1] neg_lo:[1,0,0] neg_hi:[1,0,0]
	v_pk_fma_f16 v8, v4, v140, v141 op_sel:[0,1,1] op_sel_hi:[1,1,1] neg_lo:[1,0,0] neg_hi:[1,0,0]
	v_pk_fma_f16 v9, v5, v140, v141 op_sel:[0,1,1] op_sel_hi:[1,1,1] neg_lo:[1,0,0] neg_hi:[1,0,0]
	v_mfma_f32_16x16x32_f16 v[18:21], v[10:13], v[2:5], 0
	ds_read2_b64 v[48:51], v32 offset0:16 offset1:218
	ds_read_b128 v[120:123], v33 offset:128
	ds_read2_b64 v[14:17], v34 offset0:16 offset1:218
	v_pk_fma_f16 v2, v88, v6, v2
	v_pk_fma_f16 v3, v89, v7, v3
	v_pk_fma_f16 v4, v90, v8, v4
	v_pk_fma_f16 v5, v91, v9, v5
	v_cndmask_b32_e64 v27, v27, v23, s[64:65]
	v_pk_fma_f16 v6, v2, v142, v143 op_sel:[0,1,1] op_sel_hi:[1,1,1] neg_lo:[1,0,0] neg_hi:[1,0,0]
	v_pk_fma_f16 v7, v3, v142, v143 op_sel:[0,1,1] op_sel_hi:[1,1,1] neg_lo:[1,0,0] neg_hi:[1,0,0]
	v_pk_fma_f16 v8, v4, v142, v143 op_sel:[0,1,1] op_sel_hi:[1,1,1] neg_lo:[1,0,0] neg_hi:[1,0,0]
	v_pk_fma_f16 v9, v5, v142, v143 op_sel:[0,1,1] op_sel_hi:[1,1,1] neg_lo:[1,0,0] neg_hi:[1,0,0]
	v_mfma_f32_16x16x32_f16 v[22:25], v[10:13], v[2:5], 0
	ds_read2_b64 v[52:55], v32 offset0:17 offset1:219
	v_pk_fma_f16 v2, v92, v6, v2
	v_pk_fma_f16 v3, v93, v7, v3
	v_pk_fma_f16 v4, v94, v8, v4
	v_pk_fma_f16 v5, v95, v9, v5
	v_cndmask_b32_e64 v28, v28, v20, s[64:65]
	s_waitcnt lgkmcnt(7)
	v_pk_fma_f16 v6, v2, v144, v145 op_sel:[0,1,1] op_sel_hi:[1,1,1] neg_lo:[1,0,0] neg_hi:[1,0,0]
	v_pk_fma_f16 v7, v3, v144, v145 op_sel:[0,1,1] op_sel_hi:[1,1,1] neg_lo:[1,0,0] neg_hi:[1,0,0]
	v_pk_fma_f16 v8, v4, v144, v145 op_sel:[0,1,1] op_sel_hi:[1,1,1] neg_lo:[1,0,0] neg_hi:[1,0,0]
	v_pk_fma_f16 v9, v5, v144, v145 op_sel:[0,1,1] op_sel_hi:[1,1,1] neg_lo:[1,0,0] neg_hi:[1,0,0]
	v_mfma_f32_16x16x32_f16 v[18:21], v[10:13], v[2:5], 0
	ds_read2_b64 v[56:59], v32 offset0:18 offset1:220
	ds_read_b128 v[124:127], v33 offset:144
	v_pk_fma_f16 v2, v96, v6, v2
	v_pk_fma_f16 v3, v97, v7, v3
	v_pk_fma_f16 v4, v98, v8, v4
	v_pk_fma_f16 v5, v99, v9, v5
	v_cndmask_b32_e64 v29, v29, v25, s[64:65]
	v_pk_fma_f16 v6, v2, v146, v147 op_sel:[0,1,1] op_sel_hi:[1,1,1] neg_lo:[1,0,0] neg_hi:[1,0,0]
	v_pk_fma_f16 v7, v3, v146, v147 op_sel:[0,1,1] op_sel_hi:[1,1,1] neg_lo:[1,0,0] neg_hi:[1,0,0]
	v_pk_fma_f16 v8, v4, v146, v147 op_sel:[0,1,1] op_sel_hi:[1,1,1] neg_lo:[1,0,0] neg_hi:[1,0,0]
	v_pk_fma_f16 v9, v5, v146, v147 op_sel:[0,1,1] op_sel_hi:[1,1,1] neg_lo:[1,0,0] neg_hi:[1,0,0]
	v_mfma_f32_16x16x32_f16 v[22:25], v[10:13], v[2:5], 0
	ds_read2_b64 v[60:63], v32 offset0:19 offset1:221
	v_pk_fma_f16 v2, v100, v6, v2
	v_pk_fma_f16 v3, v101, v7, v3
	v_pk_fma_f16 v4, v102, v8, v4
	v_pk_fma_f16 v5, v103, v9, v5
	v_cndmask_b32_e64 v26, v26, v18, s[66:67]
	s_waitcnt lgkmcnt(7)
	v_pk_fma_f16 v6, v2, v148, v149 op_sel:[0,1,1] op_sel_hi:[1,1,1] neg_lo:[1,0,0] neg_hi:[1,0,0]
	v_pk_fma_f16 v7, v3, v148, v149 op_sel:[0,1,1] op_sel_hi:[1,1,1] neg_lo:[1,0,0] neg_hi:[1,0,0]
	v_pk_fma_f16 v8, v4, v148, v149 op_sel:[0,1,1] op_sel_hi:[1,1,1] neg_lo:[1,0,0] neg_hi:[1,0,0]
	v_pk_fma_f16 v9, v5, v148, v149 op_sel:[0,1,1] op_sel_hi:[1,1,1] neg_lo:[1,0,0] neg_hi:[1,0,0]
	v_mfma_f32_16x16x32_f16 v[18:21], v[10:13], v[2:5], 0
	ds_read2_b64 v[64:67], v32 offset0:20 offset1:222
	ds_read_b128 v[128:131], v33 offset:160
	v_pk_fma_f16 v2, v104, v6, v2
	v_pk_fma_f16 v3, v105, v7, v3
	v_pk_fma_f16 v4, v106, v8, v4
	v_pk_fma_f16 v5, v107, v9, v5
	v_cndmask_b32_e64 v27, v27, v23, s[66:67]
	v_pk_fma_f16 v6, v2, v150, v151 op_sel:[0,1,1] op_sel_hi:[1,1,1] neg_lo:[1,0,0] neg_hi:[1,0,0]
	v_pk_fma_f16 v7, v3, v150, v151 op_sel:[0,1,1] op_sel_hi:[1,1,1] neg_lo:[1,0,0] neg_hi:[1,0,0]
	v_pk_fma_f16 v8, v4, v150, v151 op_sel:[0,1,1] op_sel_hi:[1,1,1] neg_lo:[1,0,0] neg_hi:[1,0,0]
	v_pk_fma_f16 v9, v5, v150, v151 op_sel:[0,1,1] op_sel_hi:[1,1,1] neg_lo:[1,0,0] neg_hi:[1,0,0]
	v_mfma_f32_16x16x32_f16 v[22:25], v[10:13], v[2:5], 0
	ds_read2_b64 v[68:71], v32 offset0:21 offset1:223
	v_pk_fma_f16 v2, v108, v6, v2
	v_pk_fma_f16 v3, v109, v7, v3
	v_pk_fma_f16 v4, v110, v8, v4
	v_pk_fma_f16 v5, v111, v9, v5
	v_cndmask_b32_e64 v28, v28, v20, s[66:67]
	s_waitcnt lgkmcnt(6)
	v_pk_fma_f16 v6, v2, v120, v121 op_sel:[0,1,1] op_sel_hi:[1,1,1] neg_lo:[1,0,0] neg_hi:[1,0,0]
	v_pk_fma_f16 v7, v3, v120, v121 op_sel:[0,1,1] op_sel_hi:[1,1,1] neg_lo:[1,0,0] neg_hi:[1,0,0]
	v_pk_fma_f16 v8, v4, v120, v121 op_sel:[0,1,1] op_sel_hi:[1,1,1] neg_lo:[1,0,0] neg_hi:[1,0,0]
	v_pk_fma_f16 v9, v5, v120, v121 op_sel:[0,1,1] op_sel_hi:[1,1,1] neg_lo:[1,0,0] neg_hi:[1,0,0]
	v_mfma_f32_16x16x32_f16 v[18:21], v[14:17], v[2:5], 0
	ds_read2_b64 v[72:75], v32 offset0:22 offset1:224
	ds_read_b128 v[132:135], v33 offset:176
	ds_read_b32 v37, v36 offset:8
	ds_read_b32 v38, v36 offset:72
	v_pk_fma_f16 v2, v48, v6, v2
	v_pk_fma_f16 v3, v49, v7, v3
	v_pk_fma_f16 v4, v50, v8, v4
	v_pk_fma_f16 v5, v51, v9, v5
	v_cndmask_b32_e64 v29, v29, v25, s[66:67]
	v_cvt_pk_f16_f32 v30, v26, v27
	v_cvt_pk_f16_f32 v31, v28, v29
	global_store_short v35, v30, s[68:69]
	global_store_short_d16_hi v35, v30, s[68:69] offset:64
	global_store_short v35, v31, s[68:69] offset:128
	global_store_short_d16_hi v35, v31, s[68:69] offset:192
	v_add_u32_e32 v35, 0x400, v35
	v_pk_fma_f16 v6, v2, v122, v123 op_sel:[0,1,1] op_sel_hi:[1,1,1] neg_lo:[1,0,0] neg_hi:[1,0,0]
	v_pk_fma_f16 v7, v3, v122, v123 op_sel:[0,1,1] op_sel_hi:[1,1,1] neg_lo:[1,0,0] neg_hi:[1,0,0]
	v_pk_fma_f16 v8, v4, v122, v123 op_sel:[0,1,1] op_sel_hi:[1,1,1] neg_lo:[1,0,0] neg_hi:[1,0,0]
	v_pk_fma_f16 v9, v5, v122, v123 op_sel:[0,1,1] op_sel_hi:[1,1,1] neg_lo:[1,0,0] neg_hi:[1,0,0]
	v_mfma_f32_16x16x32_f16 v[22:25], v[14:17], v[2:5], 0
	ds_read2_b64 v[76:79], v32 offset0:23 offset1:225
	v_pk_fma_f16 v2, v52, v6, v2
	v_pk_fma_f16 v3, v53, v7, v3
	v_pk_fma_f16 v4, v54, v8, v4
	v_pk_fma_f16 v5, v55, v9, v5
	v_cndmask_b32_e64 v26, v26, v18, s[60:61]
	s_waitcnt lgkmcnt(8)
	v_pk_fma_f16 v6, v2, v124, v125 op_sel:[0,1,1] op_sel_hi:[1,1,1] neg_lo:[1,0,0] neg_hi:[1,0,0]
	v_pk_fma_f16 v7, v3, v124, v125 op_sel:[0,1,1] op_sel_hi:[1,1,1] neg_lo:[1,0,0] neg_hi:[1,0,0]
	v_pk_fma_f16 v8, v4, v124, v125 op_sel:[0,1,1] op_sel_hi:[1,1,1] neg_lo:[1,0,0] neg_hi:[1,0,0]
	v_pk_fma_f16 v9, v5, v124, v125 op_sel:[0,1,1] op_sel_hi:[1,1,1] neg_lo:[1,0,0] neg_hi:[1,0,0]
	v_mfma_f32_16x16x32_f16 v[18:21], v[14:17], v[2:5], 0
	ds_read2_b64 v[80:83], v32 offset0:24 offset1:226
	ds_read_b128 v[136:139], v33 offset:192
	v_pk_fma_f16 v2, v56, v6, v2
	v_pk_fma_f16 v3, v57, v7, v3
	v_pk_fma_f16 v4, v58, v8, v4
	v_pk_fma_f16 v5, v59, v9, v5
	v_cndmask_b32_e64 v27, v27, v23, s[60:61]
	v_pk_fma_f16 v6, v2, v126, v127 op_sel:[0,1,1] op_sel_hi:[1,1,1] neg_lo:[1,0,0] neg_hi:[1,0,0]
	v_pk_fma_f16 v7, v3, v126, v127 op_sel:[0,1,1] op_sel_hi:[1,1,1] neg_lo:[1,0,0] neg_hi:[1,0,0]
	v_pk_fma_f16 v8, v4, v126, v127 op_sel:[0,1,1] op_sel_hi:[1,1,1] neg_lo:[1,0,0] neg_hi:[1,0,0]
	v_pk_fma_f16 v9, v5, v126, v127 op_sel:[0,1,1] op_sel_hi:[1,1,1] neg_lo:[1,0,0] neg_hi:[1,0,0]
	v_mfma_f32_16x16x32_f16 v[22:25], v[14:17], v[2:5], 0
	ds_read2_b64 v[84:87], v32 offset0:25 offset1:227
	v_pk_fma_f16 v2, v60, v6, v2
	v_pk_fma_f16 v3, v61, v7, v3
	v_pk_fma_f16 v4, v62, v8, v4
	v_pk_fma_f16 v5, v63, v9, v5
	v_cndmask_b32_e64 v28, v28, v20, s[60:61]
	s_waitcnt lgkmcnt(8)
	v_pk_fma_f16 v6, v2, v128, v129 op_sel:[0,1,1] op_sel_hi:[1,1,1] neg_lo:[1,0,0] neg_hi:[1,0,0]
	v_pk_fma_f16 v7, v3, v128, v129 op_sel:[0,1,1] op_sel_hi:[1,1,1] neg_lo:[1,0,0] neg_hi:[1,0,0]
	v_pk_fma_f16 v8, v4, v128, v129 op_sel:[0,1,1] op_sel_hi:[1,1,1] neg_lo:[1,0,0] neg_hi:[1,0,0]
	v_pk_fma_f16 v9, v5, v128, v129 op_sel:[0,1,1] op_sel_hi:[1,1,1] neg_lo:[1,0,0] neg_hi:[1,0,0]
	v_mfma_f32_16x16x32_f16 v[18:21], v[14:17], v[2:5], 0
	ds_read2_b64 v[88:91], v32 offset0:26 offset1:228
	ds_read_b128 v[140:143], v33 offset:208
	v_pk_fma_f16 v2, v64, v6, v2
	v_pk_fma_f16 v3, v65, v7, v3
	v_pk_fma_f16 v4, v66, v8, v4
	v_pk_fma_f16 v5, v67, v9, v5
	v_cndmask_b32_e64 v29, v29, v25, s[60:61]
	v_pk_fma_f16 v6, v2, v130, v131 op_sel:[0,1,1] op_sel_hi:[1,1,1] neg_lo:[1,0,0] neg_hi:[1,0,0]
	v_pk_fma_f16 v7, v3, v130, v131 op_sel:[0,1,1] op_sel_hi:[1,1,1] neg_lo:[1,0,0] neg_hi:[1,0,0]
	v_pk_fma_f16 v8, v4, v130, v131 op_sel:[0,1,1] op_sel_hi:[1,1,1] neg_lo:[1,0,0] neg_hi:[1,0,0]
	v_pk_fma_f16 v9, v5, v130, v131 op_sel:[0,1,1] op_sel_hi:[1,1,1] neg_lo:[1,0,0] neg_hi:[1,0,0]
	v_mfma_f32_16x16x32_f16 v[22:25], v[14:17], v[2:5], 0
	ds_read2_b64 v[92:95], v32 offset0:27 offset1:229
	v_pk_fma_f16 v2, v68, v6, v2
	v_pk_fma_f16 v3, v69, v7, v3
	v_pk_fma_f16 v4, v70, v8, v4
	v_pk_fma_f16 v5, v71, v9, v5
	v_cndmask_b32_e64 v26, v26, v18, s[62:63]
	s_waitcnt lgkmcnt(6)
	v_pk_fma_f16 v6, v2, v132, v133 op_sel:[0,1,1] op_sel_hi:[1,1,1] neg_lo:[1,0,0] neg_hi:[1,0,0]
	v_pk_fma_f16 v7, v3, v132, v133 op_sel:[0,1,1] op_sel_hi:[1,1,1] neg_lo:[1,0,0] neg_hi:[1,0,0]
	v_pk_fma_f16 v8, v4, v132, v133 op_sel:[0,1,1] op_sel_hi:[1,1,1] neg_lo:[1,0,0] neg_hi:[1,0,0]
	v_pk_fma_f16 v9, v5, v132, v133 op_sel:[0,1,1] op_sel_hi:[1,1,1] neg_lo:[1,0,0] neg_hi:[1,0,0]
	v_mfma_f32_16x16x32_f16 v[18:21], v[14:17], v[2:5], 0
	ds_read2_b64 v[96:99], v32 offset0:28 offset1:230
	ds_read_b128 v[144:147], v33 offset:224
	v_pk_fma_f16 v2, v72, v6, v2
	v_pk_fma_f16 v3, v73, v7, v3
	v_pk_fma_f16 v4, v74, v8, v4
	v_pk_fma_f16 v5, v75, v9, v5
	v_cndmask_b32_e64 v27, v27, v23, s[62:63]
	v_pk_fma_f16 v6, v2, v134, v135 op_sel:[0,1,1] op_sel_hi:[1,1,1] neg_lo:[1,0,0] neg_hi:[1,0,0]
	v_pk_fma_f16 v7, v3, v134, v135 op_sel:[0,1,1] op_sel_hi:[1,1,1] neg_lo:[1,0,0] neg_hi:[1,0,0]
	v_pk_fma_f16 v8, v4, v134, v135 op_sel:[0,1,1] op_sel_hi:[1,1,1] neg_lo:[1,0,0] neg_hi:[1,0,0]
	v_pk_fma_f16 v9, v5, v134, v135 op_sel:[0,1,1] op_sel_hi:[1,1,1] neg_lo:[1,0,0] neg_hi:[1,0,0]
	v_mfma_f32_16x16x32_f16 v[22:25], v[14:17], v[2:5], 0
	ds_read2_b64 v[100:103], v32 offset0:29 offset1:231
	v_pk_fma_f16 v2, v76, v6, v2
	v_pk_fma_f16 v3, v77, v7, v3
	v_pk_fma_f16 v4, v78, v8, v4
	v_pk_fma_f16 v5, v79, v9, v5
	v_cndmask_b32_e64 v28, v28, v20, s[62:63]
	s_waitcnt lgkmcnt(6)
	v_pk_fma_f16 v6, v2, v136, v137 op_sel:[0,1,1] op_sel_hi:[1,1,1] neg_lo:[1,0,0] neg_hi:[1,0,0]
	v_pk_fma_f16 v7, v3, v136, v137 op_sel:[0,1,1] op_sel_hi:[1,1,1] neg_lo:[1,0,0] neg_hi:[1,0,0]
	v_pk_fma_f16 v8, v4, v136, v137 op_sel:[0,1,1] op_sel_hi:[1,1,1] neg_lo:[1,0,0] neg_hi:[1,0,0]
	v_pk_fma_f16 v9, v5, v136, v137 op_sel:[0,1,1] op_sel_hi:[1,1,1] neg_lo:[1,0,0] neg_hi:[1,0,0]
	v_mfma_f32_16x16x32_f16 v[18:21], v[14:17], v[2:5], 0
	ds_read2_b64 v[104:107], v32 offset0:30 offset1:232
	ds_read_b128 v[148:151], v33 offset:240
	v_pk_fma_f16 v2, v80, v6, v2
	v_pk_fma_f16 v3, v81, v7, v3
	v_pk_fma_f16 v4, v82, v8, v4
	v_pk_fma_f16 v5, v83, v9, v5
	v_cndmask_b32_e64 v29, v29, v25, s[62:63]
	v_readfirstlane_b32 s4, v37
	v_readfirstlane_b32 s5, v38
	s_and_b32 s4, s4, s5
	s_cbranch_scc0 .Lc1_slow1
.Lc1_back1:
	v_pk_fma_f16 v6, v2, v138, v139 op_sel:[0,1,1] op_sel_hi:[1,1,1] neg_lo:[1,0,0] neg_hi:[1,0,0]
	v_pk_fma_f16 v7, v3, v138, v139 op_sel:[0,1,1] op_sel_hi:[1,1,1] neg_lo:[1,0,0] neg_hi:[1,0,0]
	v_pk_fma_f16 v8, v4, v138, v139 op_sel:[0,1,1] op_sel_hi:[1,1,1] neg_lo:[1,0,0] neg_hi:[1,0,0]
	v_pk_fma_f16 v9, v5, v138, v139 op_sel:[0,1,1] op_sel_hi:[1,1,1] neg_lo:[1,0,0] neg_hi:[1,0,0]
	v_mfma_f32_16x16x32_f16 v[22:25], v[14:17], v[2:5], 0
	ds_read2_b64 v[108:111], v32 offset0:31 offset1:233
	v_pk_fma_f16 v2, v84, v6, v2
	v_pk_fma_f16 v3, v85, v7, v3
	v_pk_fma_f16 v4, v86, v8, v4
	v_pk_fma_f16 v5, v87, v9, v5
	v_cndmask_b32_e64 v26, v26, v18, s[64:65]
	s_waitcnt lgkmcnt(6)
	v_pk_fma_f16 v6, v2, v140, v141 op_sel:[0,1,1] op_sel_hi:[1,1,1] neg_lo:[1,0,0] neg_hi:[1,0,0]
	v_pk_fma_f16 v7, v3, v140, v141 op_sel:[0,1,1] op_sel_hi:[1,1,1] neg_lo:[1,0,0] neg_hi:[1,0,0]
	v_pk_fma_f16 v8, v4, v140, v141 op_sel:[0,1,1] op_sel_hi:[1,1,1] neg_lo:[1,0,0] neg_hi:[1,0,0]
	v_pk_fma_f16 v9, v5, v140, v141 op_sel:[0,1,1] op_sel_hi:[1,1,1] neg_lo:[1,0,0] neg_hi:[1,0,0]
	v_mfma_f32_16x16x32_f16 v[18:21], v[14:17], v[2:5], 0
	ds_read2_b64 v[48:51], v32 offset0:32 offset1:234
	ds_read_b128 v[120:123], v33 offset:256
	ds_read2_b64 v[10:13], v34 offset0:32 offset1:234
	v_pk_fma_f16 v2, v88, v6, v2
	v_pk_fma_f16 v3, v89, v7, v3
	v_pk_fma_f16 v4, v90, v8, v4
	v_pk_fma_f16 v5, v91, v9, v5
	v_cndmask_b32_e64 v27, v27, v23, s[64:65]
	v_pk_fma_f16 v6, v2, v142, v143 op_sel:[0,1,1] op_sel_hi:[1,1,1] neg_lo:[1,0,0] neg_hi:[1,0,0]
	v_pk_fma_f16 v7, v3, v142, v143 op_sel:[0,1,1] op_sel_hi:[1,1,1] neg_lo:[1,0,0] neg_hi:[1,0,0]
	v_pk_fma_f16 v8, v4, v142, v143 op_sel:[0,1,1] op_sel_hi:[1,1,1] neg_lo:[1,0,0] neg_hi:[1,0,0]
	v_pk_fma_f16 v9, v5, v142, v143 op_sel:[0,1,1] op_sel_hi:[1,1,1] neg_lo:[1,0,0] neg_hi:[1,0,0]
	v_mfma_f32_16x16x32_f16 v[22:25], v[14:17], v[2:5], 0
	ds_read2_b64 v[52:55], v32 offset0:33 offset1:235
	v_pk_fma_f16 v2, v92, v6, v2
	v_pk_fma_f16 v3, v93, v7, v3
	v_pk_fma_f16 v4, v94, v8, v4
	v_pk_fma_f16 v5, v95, v9, v5
	v_cndmask_b32_e64 v28, v28, v20, s[64:65]
	s_waitcnt lgkmcnt(7)
	v_pk_fma_f16 v6, v2, v144, v145 op_sel:[0,1,1] op_sel_hi:[1,1,1] neg_lo:[1,0,0] neg_hi:[1,0,0]
	v_pk_fma_f16 v7, v3, v144, v145 op_sel:[0,1,1] op_sel_hi:[1,1,1] neg_lo:[1,0,0] neg_hi:[1,0,0]
	v_pk_fma_f16 v8, v4, v144, v145 op_sel:[0,1,1] op_sel_hi:[1,1,1] neg_lo:[1,0,0] neg_hi:[1,0,0]
	v_pk_fma_f16 v9, v5, v144, v145 op_sel:[0,1,1] op_sel_hi:[1,1,1] neg_lo:[1,0,0] neg_hi:[1,0,0]
	v_mfma_f32_16x16x32_f16 v[18:21], v[14:17], v[2:5], 0
	ds_read2_b64 v[56:59], v32 offset0:34 offset1:236
	ds_read_b128 v[124:127], v33 offset:272
	v_pk_fma_f16 v2, v96, v6, v2
	v_pk_fma_f16 v3, v97, v7, v3
	v_pk_fma_f16 v4, v98, v8, v4
	v_pk_fma_f16 v5, v99, v9, v5
	v_cndmask_b32_e64 v29, v29, v25, s[64:65]
	v_pk_fma_f16 v6, v2, v146, v147 op_sel:[0,1,1] op_sel_hi:[1,1,1] neg_lo:[1,0,0] neg_hi:[1,0,0]
	v_pk_fma_f16 v7, v3, v146, v147 op_sel:[0,1,1] op_sel_hi:[1,1,1] neg_lo:[1,0,0] neg_hi:[1,0,0]
	v_pk_fma_f16 v8, v4, v146, v147 op_sel:[0,1,1] op_sel_hi:[1,1,1] neg_lo:[1,0,0] neg_hi:[1,0,0]
	v_pk_fma_f16 v9, v5, v146, v147 op_sel:[0,1,1] op_sel_hi:[1,1,1] neg_lo:[1,0,0] neg_hi:[1,0,0]
	v_mfma_f32_16x16x32_f16 v[22:25], v[14:17], v[2:5], 0
	ds_read2_b64 v[60:63], v32 offset0:35 offset1:237
	v_pk_fma_f16 v2, v100, v6, v2
	v_pk_fma_f16 v3, v101, v7, v3
	v_pk_fma_f16 v4, v102, v8, v4
	v_pk_fma_f16 v5, v103, v9, v5
	v_cndmask_b32_e64 v26, v26, v18, s[66:67]
	s_waitcnt lgkmcnt(7)
	v_pk_fma_f16 v6, v2, v148, v149 op_sel:[0,1,1] op_sel_hi:[1,1,1] neg_lo:[1,0,0] neg_hi:[1,0,0]
	v_pk_fma_f16 v7, v3, v148, v149 op_sel:[0,1,1] op_sel_hi:[1,1,1] neg_lo:[1,0,0] neg_hi:[1,0,0]
	v_pk_fma_f16 v8, v4, v148, v149 op_sel:[0,1,1] op_sel_hi:[1,1,1] neg_lo:[1,0,0] neg_hi:[1,0,0]
	v_pk_fma_f16 v9, v5, v148, v149 op_sel:[0,1,1] op_sel_hi:[1,1,1] neg_lo:[1,0,0] neg_hi:[1,0,0]
	v_mfma_f32_16x16x32_f16 v[18:21], v[14:17], v[2:5], 0
	ds_read2_b64 v[64:67], v32 offset0:36 offset1:238
	ds_read_b128 v[128:131], v33 offset:288
	v_pk_fma_f16 v2, v104, v6, v2
	v_pk_fma_f16 v3, v105, v7, v3
	v_pk_fma_f16 v4, v106, v8, v4
	v_pk_fma_f16 v5, v107, v9, v5
	v_cndmask_b32_e64 v27, v27, v23, s[66:67]
	v_pk_fma_f16 v6, v2, v150, v151 op_sel:[0,1,1] op_sel_hi:[1,1,1] neg_lo:[1,0,0] neg_hi:[1,0,0]
	v_pk_fma_f16 v7, v3, v150, v151 op_sel:[0,1,1] op_sel_hi:[1,1,1] neg_lo:[1,0,0] neg_hi:[1,0,0]
	v_pk_fma_f16 v8, v4, v150, v151 op_sel:[0,1,1] op_sel_hi:[1,1,1] neg_lo:[1,0,0] neg_hi:[1,0,0]
	v_pk_fma_f16 v9, v5, v150, v151 op_sel:[0,1,1] op_sel_hi:[1,1,1] neg_lo:[1,0,0] neg_hi:[1,0,0]
	v_mfma_f32_16x16x32_f16 v[22:25], v[14:17], v[2:5], 0
	ds_read2_b64 v[68:71], v32 offset0:37 offset1:239
	v_pk_fma_f16 v2, v108, v6, v2
	v_pk_fma_f16 v3, v109, v7, v3
	v_pk_fma_f16 v4, v110, v8, v4
	v_pk_fma_f16 v5, v111, v9, v5
	v_cndmask_b32_e64 v28, v28, v20, s[66:67]
	v_add_u32_e32 v32, 0x100, v32
	v_add_u32_e32 v33, 0x100, v33
	v_add_u32_e32 v34, 0x100, v34
	v_add_u32_e32 v36, 8, v36
	s_add_i32 s70, s70, 1
	s_cmp_lt_u32 s70, 6
	s_cbranch_scc1 .Lc1_loop
	s_waitcnt lgkmcnt(6)
	v_pk_fma_f16 v6, v2, v120, v121 op_sel:[0,1,1] op_sel_hi:[1,1,1] neg_lo:[1,0,0] neg_hi:[1,0,0]
	v_pk_fma_f16 v7, v3, v120, v121 op_sel:[0,1,1] op_sel_hi:[1,1,1] neg_lo:[1,0,0] neg_hi:[1,0,0]
	v_pk_fma_f16 v8, v4, v120, v121 op_sel:[0,1,1] op_sel_hi:[1,1,1] neg_lo:[1,0,0] neg_hi:[1,0,0]
	v_pk_fma_f16 v9, v5, v120, v121 op_sel:[0,1,1] op_sel_hi:[1,1,1] neg_lo:[1,0,0] neg_hi:[1,0,0]
	v_mfma_f32_16x16x32_f16 v[18:21], v[10:13], v[2:5], 0
	ds_read2_b64 v[72:75], v32 offset0:6 offset1:208
	ds_read_b128 v[132:135], v33 offset:48
	v_pk_fma_f16 v2, v48, v6, v2
	v_pk_fma_f16 v3, v49, v7, v3
	v_pk_fma_f16 v4, v50, v8, v4
	v_pk_fma_f16 v5, v51, v9, v5
	v_cndmask_b32_e64 v29, v29, v25, s[66:67]
	v_cvt_pk_f16_f32 v30, v26, v27
	v_cvt_pk_f16_f32 v31, v28, v29
	global_store_short v35, v30, s[68:69]
	global_store_short_d16_hi v35, v30, s[68:69] offset:64
	global_store_short v35, v31, s[68:69] offset:128
	global_store_short_d16_hi v35, v31, s[68:69] offset:192
	v_add_u32_e32 v35, 0x400, v35
	v_pk_fma_f16 v6, v2, v122, v123 op_sel:[0,1,1] op_sel_hi:[1,1,1] neg_lo:[1,0,0] neg_hi:[1,0,0]
	v_pk_fma_f16 v7, v3, v122, v123 op_sel:[0,1,1] op_sel_hi:[1,1,1] neg_lo:[1,0,0] neg_hi:[1,0,0]
	v_pk_fma_f16 v8, v4, v122, v123 op_sel:[0,1,1] op_sel_hi:[1,1,1] neg_lo:[1,0,0] neg_hi:[1,0,0]
	v_pk_fma_f16 v9, v5, v122, v123 op_sel:[0,1,1] op_sel_hi:[1,1,1] neg_lo:[1,0,0] neg_hi:[1,0,0]
	v_mfma_f32_16x16x32_f16 v[22:25], v[10:13], v[2:5], 0
	ds_read2_b64 v[76:79], v32 offset0:7 offset1:209
	v_pk_fma_f16 v2, v52, v6, v2
	v_pk_fma_f16 v3, v53, v7, v3
	v_pk_fma_f16 v4, v54, v8, v4
	v_pk_fma_f16 v5, v55, v9, v5
	v_cndmask_b32_e64 v26, v26, v18, s[60:61]
	s_waitcnt lgkmcnt(6)
	v_pk_fma_f16 v6, v2, v124, v125 op_sel:[0,1,1] op_sel_hi:[1,1,1] neg_lo:[1,0,0] neg_hi:[1,0,0]
	v_pk_fma_f16 v7, v3, v124, v125 op_sel:[0,1,1] op_sel_hi:[1,1,1] neg_lo:[1,0,0] neg_hi:[1,0,0]
	v_pk_fma_f16 v8, v4, v124, v125 op_sel:[0,1,1] op_sel_hi:[1,1,1] neg_lo:[1,0,0] neg_hi:[1,0,0]
	v_pk_fma_f16 v9, v5, v124, v125 op_sel:[0,1,1] op_sel_hi:[1,1,1] neg_lo:[1,0,0] neg_hi:[1,0,0]
	v_mfma_f32_16x16x32_f16 v[18:21], v[10:13], v[2:5], 0
	v_pk_fma_f16 v2, v56, v6, v2
	v_pk_fma_f16 v3, v57, v7, v3
	v_pk_fma_f16 v4, v58, v8, v4
	v_pk_fma_f16 v5, v59, v9, v5
	v_cndmask_b32_e64 v27, v27, v23, s[60:61]
	v_pk_fma_f16 v6, v2, v126, v127 op_sel:[0,1,1] op_sel_hi:[1,1,1] neg_lo:[1,0,0] neg_hi:[1,0,0]
	v_pk_fma_f16 v7, v3, v126, v127 op_sel:[0,1,1] op_sel_hi:[1,1,1] neg_lo:[1,0,0] neg_hi:[1,0,0]
	v_pk_fma_f16 v8, v4, v126, v127 op_sel:[0,1,1] op_sel_hi:[1,1,1] neg_lo:[1,0,0] neg_hi:[1,0,0]
	v_pk_fma_f16 v9, v5, v126, v127 op_sel:[0,1,1] op_sel_hi:[1,1,1] neg_lo:[1,0,0] neg_hi:[1,0,0]
	v_mfma_f32_16x16x32_f16 v[22:25], v[10:13], v[2:5], 0
	v_pk_fma_f16 v2, v60, v6, v2
	v_pk_fma_f16 v3, v61, v7, v3
	v_pk_fma_f16 v4, v62, v8, v4
	v_pk_fma_f16 v5, v63, v9, v5
	v_cndmask_b32_e64 v28, v28, v20, s[60:61]
	s_waitcnt lgkmcnt(3)
	v_pk_fma_f16 v6, v2, v128, v129 op_sel:[0,1,1] op_sel_hi:[1,1,1] neg_lo:[1,0,0] neg_hi:[1,0,0]
	v_pk_fma_f16 v7, v3, v128, v129 op_sel:[0,1,1] op_sel_hi:[1,1,1] neg_lo:[1,0,0] neg_hi:[1,0,0]
	v_pk_fma_f16 v8, v4, v128, v129 op_sel:[0,1,1] op_sel_hi:[1,1,1] neg_lo:[1,0,0] neg_hi:[1,0,0]
	v_pk_fma_f16 v9, v5, v128, v129 op_sel:[0,1,1] op_sel_hi:[1,1,1] neg_lo:[1,0,0] neg_hi:[1,0,0]
	v_mfma_f32_16x16x32_f16 v[18:21], v[10:13], v[2:5], 0
	v_pk_fma_f16 v2, v64, v6, v2
	v_pk_fma_f16 v3, v65, v7, v3
	v_pk_fma_f16 v4, v66, v8, v4
	v_pk_fma_f16 v5, v67, v9, v5
	v_cndmask_b32_e64 v29, v29, v25, s[60:61]
	v_pk_fma_f16 v6, v2, v130, v131 op_sel:[0,1,1] op_sel_hi:[1,1,1] neg_lo:[1,0,0] neg_hi:[1,0,0]
	v_pk_fma_f16 v7, v3, v130, v131 op_sel:[0,1,1] op_sel_hi:[1,1,1] neg_lo:[1,0,0] neg_hi:[1,0,0]
	v_pk_fma_f16 v8, v4, v130, v131 op_sel:[0,1,1] op_sel_hi:[1,1,1] neg_lo:[1,0,0] neg_hi:[1,0,0]
	v_pk_fma_f16 v9, v5, v130, v131 op_sel:[0,1,1] op_sel_hi:[1,1,1] neg_lo:[1,0,0] neg_hi:[1,0,0]
	v_mfma_f32_16x16x32_f16 v[22:25], v[10:13], v[2:5], 0
	v_pk_fma_f16 v2, v68, v6, v2
	v_pk_fma_f16 v3, v69, v7, v3
	v_pk_fma_f16 v4, v70, v8, v4
	v_pk_fma_f16 v5, v71, v9, v5
	v_cndmask_b32_e64 v26, v26, v18, s[62:63]
	s_waitcnt lgkmcnt(0)
	v_pk_fma_f16 v6, v2, v132, v133 op_sel:[0,1,1] op_sel_hi:[1,1,1] neg_lo:[1,0,0] neg_hi:[1,0,0]
	v_pk_fma_f16 v7, v3, v132, v133 op_sel:[0,1,1] op_sel_hi:[1,1,1] neg_lo:[1,0,0] neg_hi:[1,0,0]
	v_pk_fma_f16 v8, v4, v132, v133 op_sel:[0,1,1] op_sel_hi:[1,1,1] neg_lo:[1,0,0] neg_hi:[1,0,0]
	v_pk_fma_f16 v9, v5, v132, v133 op_sel:[0,1,1] op_sel_hi:[1,1,1] neg_lo:[1,0,0] neg_hi:[1,0,0]
	v_mfma_f32_16x16x32_f16 v[18:21], v[10:13], v[2:5], 0
	v_pk_fma_f16 v2, v72, v6, v2
	v_pk_fma_f16 v3, v73, v7, v3
	v_pk_fma_f16 v4, v74, v8, v4
	v_pk_fma_f16 v5, v75, v9, v5
	v_cndmask_b32_e64 v27, v27, v23, s[62:63]
	v_pk_fma_f16 v6, v2, v134, v135 op_sel:[0,1,1] op_sel_hi:[1,1,1] neg_lo:[1,0,0] neg_hi:[1,0,0]
	v_pk_fma_f16 v7, v3, v134, v135 op_sel:[0,1,1] op_sel_hi:[1,1,1] neg_lo:[1,0,0] neg_hi:[1,0,0]
	v_pk_fma_f16 v8, v4, v134, v135 op_sel:[0,1,1] op_sel_hi:[1,1,1] neg_lo:[1,0,0] neg_hi:[1,0,0]
	v_pk_fma_f16 v9, v5, v134, v135 op_sel:[0,1,1] op_sel_hi:[1,1,1] neg_lo:[1,0,0] neg_hi:[1,0,0]
	v_mfma_f32_16x16x32_f16 v[22:25], v[10:13], v[2:5], 0
	v_pk_fma_f16 v2, v76, v6, v2
	v_pk_fma_f16 v3, v77, v7, v3
	v_pk_fma_f16 v4, v78, v8, v4
	v_pk_fma_f16 v5, v79, v9, v5
	v_cndmask_b32_e64 v28, v28, v20, s[62:63]
	s_nop 7
	v_cndmask_b32_e64 v29, v29, v25, s[62:63]
	v_cvt_pk_f16_f32 v30, v26, v27
	v_cvt_pk_f16_f32 v31, v28, v29
	s_mov_b32 exec_lo, -1
	s_mov_b32 exec_hi, 0
	global_store_short v35, v30, s[68:69]
	global_store_short_d16_hi v35, v30, s[68:69] offset:64
	global_store_short v35, v31, s[68:69] offset:128
	global_store_short_d16_hi v35, v31, s[68:69] offset:192
	s_endpgm

_Z2kBPKfPKDv4_jPKDF16_S0_S0_S0_Pf:
	v_lshrrev_b32_e32 v11, 7, v0
	s_load_dwordx8 s[4:11], s[0:1], 0x0
	v_lshl_or_b32 v2, s2, 2, v11
	s_mov_b32 s2, 0x4ec4ec4f
	v_mul_hi_i32 v1, v2, s2
	v_lshrrev_b32_e32 v3, 31, v1
	v_ashrrev_i32_e32 v1, 2, v1
	v_add_u32_e32 v1, v1, v3
	v_and_b32_e32 v108, 15, v0
	v_mad_u64_u32 v[4:5], s[2:3], v1, -13, v[2:3]
	v_lshlrev_b32_e32 v102, 4, v0
	v_mov_b32_e32 v103, 0
	v_lshl_or_b32 v10, v4, 4, v108
	s_waitcnt lgkmcnt(0)
	v_lshl_add_u64 v[4:5], s[8:9], 0, v[102:103]
	s_movk_i32 s2, 0x2000
	v_add_co_u32_e32 v6, vcc, s2, v4
	s_movk_i32 s2, 0x4000
	s_nop 0
	v_addc_co_u32_e32 v7, vcc, 0, v5, vcc
	v_add_co_u32_e32 v8, vcc, s2, v4
	s_movk_i32 s2, 0x6000
	s_nop 0
	v_addc_co_u32_e32 v9, vcc, 0, v5, vcc
	global_load_dwordx4 v[14:17], v102, s[8:9]
	global_load_dwordx4 v[18:21], v[6:7], off
	global_load_dwordx4 v[22:25], v[8:9], off
	v_add_co_u32_e32 v6, vcc, s2, v4
	s_mov_b32 s2, 0x8000
	s_nop 0
	v_addc_co_u32_e32 v7, vcc, 0, v5, vcc
	v_add_co_u32_e32 v8, vcc, s2, v4
	s_mov_b32 s2, 0xa000
	s_nop 0
	v_addc_co_u32_e32 v9, vcc, 0, v5, vcc
	global_load_dwordx4 v[26:29], v[6:7], off
	global_load_dwordx4 v[30:33], v[8:9], off
	v_add_co_u32_e32 v6, vcc, s2, v4
	s_mov_b32 s2, 0xc000
	s_nop 0
	v_addc_co_u32_e32 v7, vcc, 0, v5, vcc
	v_add_co_u32_e32 v8, vcc, s2, v4
	s_mov_b32 s2, 0xe000
	s_nop 0
	v_addc_co_u32_e32 v9, vcc, 0, v5, vcc
	v_add_co_u32_e32 v4, vcc, s2, v4
	s_movk_i32 s2, 0xc8
	s_nop 0
	v_addc_co_u32_e32 v5, vcc, 0, v5, vcc
	global_load_dwordx4 v[34:37], v[6:7], off
	global_load_dwordx4 v[38:41], v[8:9], off
	v_mov_b32_e32 v3, 0xc7
	v_cmp_gt_i32_e32 vcc, s2, v10
	global_load_dwordx4 v[42:45], v[4:5], off
	s_movk_i32 s2, 0x640
	v_cndmask_b32_e32 v4, v3, v10, vcc
	v_mad_u64_u32 v[4:5], s[2:3], v1, s2, v[4:5]
	v_and_b32_e32 v6, 48, v0
	v_mov_b32_e32 v7, v103
	v_ashrrev_i32_e32 v5, 31, v4
	v_lshl_add_u64 v[8:9], s[4:5], 0, v[6:7]
	v_lshlrev_b64 v[12:13], 6, v[4:5]
	v_lshl_add_u64 v[12:13], v[8:9], 0, v[12:13]
	global_load_dwordx4 v[46:49], v[12:13], off
	s_mov_b32 s12, 0x3200
	s_mov_b32 s13, 0
	v_lshl_add_u64 v[12:13], v[12:13], 0, s[12:13]
	global_load_dwordx4 v[110:113], v[12:13], off
	v_lshl_add_u64 v[12:13], v[12:13], 0, s[12:13]
	global_load_dwordx4 v[50:53], v[12:13], off
	v_lshl_add_u64 v[12:13], v[12:13], 0, s[12:13]
	global_load_dwordx4 v[114:117], v[12:13], off
	v_lshl_add_u64 v[12:13], v[12:13], 0, s[12:13]
	global_load_dwordx4 v[54:57], v[12:13], off
	v_lshl_add_u64 v[12:13], v[12:13], 0, s[12:13]
	global_load_dwordx4 v[118:121], v[12:13], off
	v_lshl_add_u64 v[12:13], v[12:13], 0, s[12:13]
	global_load_dwordx4 v[58:61], v[12:13], off
	v_lshl_add_u64 v[12:13], v[12:13], 0, s[12:13]
	global_load_dwordx4 v[122:125], v[12:13], off
	v_and_b32_e32 v13, 63, v0
	v_lshl_or_b32 v2, v2, 8, v13
	v_ashrrev_i32_e32 v3, 31, v2
	v_lshl_add_u64 v[2:3], v[2:3], 4, s[6:7]
	global_load_dwordx4 v[62:65], v[2:3], off
	global_load_dwordx4 v[66:69], v[2:3], off offset:1024
	global_load_dwordx4 v[70:73], v[2:3], off offset:2048
	global_load_dwordx4 v[74:77], v[2:3], off offset:3072
	s_load_dwordx4 s[4:7], s[0:1], 0x20
	v_bfe_u32 v12, v0, 6, 1
	v_lshl_add_u64 v[2:3], s[10:11], 0, v[6:7]
	v_and_b32_e32 v0, 64, v0
	v_cmp_gt_u32_e64 s[2:3], 16, v13
	s_waitcnt lgkmcnt(0)
	v_lshl_add_u64 v[4:5], s[4:5], 0, v[6:7]
	v_lshlrev_b32_e32 v6, 8, v12
	v_lshl_add_u64 v[104:105], v[2:3], 0, v[6:7]
	v_lshl_add_u64 v[106:107], v[4:5], 0, v[6:7]
	global_load_dwordx4 v[78:81], v[104:105], off
	global_load_dwordx4 v[82:85], v[104:105], off offset:64
	global_load_dwordx4 v[86:89], v[106:107], off
	global_load_dwordx4 v[90:93], v[106:107], off offset:64
	global_load_dwordx4 v[94:97], v[104:105], off offset:128
	global_load_dwordx4 v[6:9], v[104:105], off offset:192
	global_load_dwordx4 v[98:101], v[106:107], off offset:128
	global_load_dwordx4 v[2:5], v[106:107], off offset:192
	s_load_dword s6, s[6:7], 0x0
	s_waitcnt vmcnt(27)
	ds_write_b128 v102, v[14:17]
	s_waitcnt vmcnt(26)
	ds_write_b128 v102, v[18:21] offset:8192
	s_waitcnt vmcnt(25)
	ds_write_b128 v102, v[22:25] offset:16384
	s_waitcnt vmcnt(24)
	ds_write_b128 v102, v[26:29] offset:24576
	s_waitcnt vmcnt(23)
	ds_write_b128 v102, v[30:33] offset:32768
	s_waitcnt vmcnt(22)
	ds_write_b128 v102, v[34:37] offset:40960
	s_waitcnt vmcnt(21)
	ds_write_b128 v102, v[38:41] offset:49152
	s_waitcnt vmcnt(20)
	ds_write_b128 v102, v[42:45] offset:57344
	v_lshlrev_b32_e32 v14, 15, v12
	v_lshl_or_b32 v38, v13, 4, v14
	s_waitcnt lgkmcnt(0)
	s_barrier
	ds_read_b128 v[14:17], v38
	ds_read_b128 v[18:21], v38 offset:1024
	s_waitcnt vmcnt(18) lgkmcnt(1)
	v_pk_add_f16 v46, v46, v110
	v_pk_add_f16 v47, v47, v111
	v_pk_add_f16 v48, v48, v112
	v_pk_add_f16 v49, v49, v113
	s_nop 1
	v_mfma_f32_16x16x32_f16 v[14:17], v[14:17], v[46:49], 0
	ds_read_b128 v[22:25], v38 offset:2048
	ds_read_b128 v[26:29], v38 offset:10240
	ds_read_b128 v[30:33], v38 offset:18432
	s_waitcnt vmcnt(16) lgkmcnt(3)
	v_pk_add_f16 v50, v50, v114
	v_pk_add_f16 v51, v51, v115
	v_pk_add_f16 v52, v52, v116
	v_pk_add_f16 v53, v53, v117
	s_nop 1
	v_mfma_f32_16x16x32_f16 v[14:17], v[18:21], v[50:53], v[14:17]
	ds_read_b128 v[18:21], v38 offset:3072
	ds_read_b128 v[34:37], v38 offset:26624
	v_cmp_ne_u32_e64 s[4:5], 0, v0
	s_waitcnt vmcnt(14) lgkmcnt(4)
	v_pk_add_f16 v54, v54, v118
	v_pk_add_f16 v55, v55, v119
	v_pk_add_f16 v56, v56, v120
	v_pk_add_f16 v57, v57, v121
	s_nop 1
	v_mfma_f32_16x16x32_f16 v[14:17], v[22:25], v[54:57], v[14:17]
	ds_read_b128 v[22:25], v38 offset:4096
	s_and_b64 s[8:9], s[4:5], s[2:3]
	v_lshlrev_b32_e32 v0, 2, v108
	s_waitcnt vmcnt(12) lgkmcnt(2)
	v_pk_add_f16 v58, v58, v122
	v_pk_add_f16 v59, v59, v123
	v_pk_add_f16 v60, v60, v124
	v_pk_add_f16 v61, v61, v125
	s_nop 1
	v_mfma_f32_16x16x32_f16 v[14:17], v[18:21], v[58:61], v[14:17]
	ds_read_b128 v[18:21], v38 offset:5120
	s_waitcnt vmcnt(11) lgkmcnt(1)
	v_mfma_f32_16x16x32_f16 v[14:17], v[22:25], v[62:65], v[14:17]
	ds_read_b128 v[22:25], v38 offset:6144
	s_waitcnt vmcnt(10) lgkmcnt(1)
	v_mfma_f32_16x16x32_f16 v[14:17], v[18:21], v[66:69], v[14:17]
	ds_read_b128 v[18:21], v38 offset:7168
	s_waitcnt vmcnt(9) lgkmcnt(1)
	v_mfma_f32_16x16x32_f16 v[14:17], v[22:25], v[70:73], v[14:17]
	ds_read_b128 v[22:25], v38 offset:8192
	s_waitcnt vmcnt(8) lgkmcnt(1)
	v_mfma_f32_16x16x32_f16 v[14:17], v[18:21], v[74:77], v[14:17]
	ds_read_b128 v[18:21], v38 offset:9216
	s_waitcnt lgkmcnt(1)
	v_mfma_f32_16x16x32_f16 v[22:25], v[22:25], v[46:49], 0
	s_waitcnt vmcnt(7)
	s_nop 3
	v_add_f32_e32 v14, v14, v78
	v_mul_f32_e32 v14, 0x4038aa3b, v14
	v_add_f32_e32 v15, v15, v79
	s_waitcnt lgkmcnt(0)
	v_mfma_f32_16x16x32_f16 v[18:21], v[18:21], v[50:53], v[22:25]
	v_exp_f32_e32 v14, v14
	v_mul_f32_e32 v15, 0x4038aa3b, v15
	s_nop 0
	ds_read_b128 v[22:25], v38 offset:11264
	v_mfma_f32_16x16x32_f16 v[18:21], v[26:29], v[54:57], v[18:21]
	ds_read_b128 v[26:29], v38 offset:12288
	v_add_f32_e32 v16, v16, v80
	v_exp_f32_e32 v15, v15
	s_waitcnt lgkmcnt(1)
	v_mfma_f32_16x16x32_f16 v[18:21], v[22:25], v[58:61], v[18:21]
	ds_read_b128 v[22:25], v38 offset:13312
	v_mul_f32_e32 v16, 0x4038aa3b, v16
	v_add_f32_e32 v17, v17, v81
	s_waitcnt lgkmcnt(1)
	v_mfma_f32_16x16x32_f16 v[18:21], v[26:29], v[62:65], v[18:21]
	ds_read_b128 v[26:29], v38 offset:14336
	v_exp_f32_e32 v16, v16
	v_mul_f32_e32 v17, 0x4038aa3b, v17
	s_waitcnt lgkmcnt(1)
	v_mfma_f32_16x16x32_f16 v[18:21], v[22:25], v[66:69], v[18:21]
	ds_read_b128 v[22:25], v38 offset:15360
	v_exp_f32_e32 v17, v17
	v_add_f32_e32 v14, 1.0, v14
	s_waitcnt lgkmcnt(1)
	v_mfma_f32_16x16x32_f16 v[18:21], v[26:29], v[70:73], v[18:21]
	ds_read_b128 v[26:29], v38 offset:16384
	v_rcp_f32_e32 v14, v14
	v_add_f32_e32 v15, 1.0, v15
	s_waitcnt lgkmcnt(1)
	v_mfma_f32_16x16x32_f16 v[18:21], v[22:25], v[74:77], v[18:21]
	ds_read_b128 v[22:25], v38 offset:17408
	v_rcp_f32_e32 v15, v15
	v_add_f32_e32 v16, 1.0, v16
	s_waitcnt lgkmcnt(1)
	v_mfma_f32_16x16x32_f16 v[26:29], v[26:29], v[46:49], 0
	v_rcp_f32_e32 v16, v16
	v_add_f32_e32 v17, 1.0, v17
	v_rcp_f32_e32 v17, v17
	s_waitcnt lgkmcnt(0)
	v_mfma_f32_16x16x32_f16 v[22:25], v[22:25], v[50:53], v[26:29]
	v_fma_f32 v14, v14, -2.0, 1.0
	s_nop 1
	ds_read_b128 v[26:29], v38 offset:19456
	s_waitcnt vmcnt(5)
	v_fma_f32 v14, v14, v86, 0
	v_mfma_f32_16x16x32_f16 v[22:25], v[30:33], v[54:57], v[22:25]
	ds_read_b128 v[30:33], v38 offset:20480
	v_fma_f32 v15, v15, -2.0, 1.0
	v_fmac_f32_e32 v14, v15, v87
	s_waitcnt lgkmcnt(1)
	v_mfma_f32_16x16x32_f16 v[22:25], v[26:29], v[58:61], v[22:25]
	ds_read_b128 v[26:29], v38 offset:21504
	v_fma_f32 v15, v16, -2.0, 1.0
	v_fmac_f32_e32 v14, v15, v88
	s_waitcnt lgkmcnt(1)
	v_mfma_f32_16x16x32_f16 v[22:25], v[30:33], v[62:65], v[22:25]
	ds_read_b128 v[30:33], v38 offset:22528
	v_fma_f32 v15, v17, -2.0, 1.0
	v_add_f32_e32 v16, v18, v82
	s_waitcnt lgkmcnt(1)
	v_mfma_f32_16x16x32_f16 v[22:25], v[26:29], v[66:69], v[22:25]
	ds_read_b128 v[26:29], v38 offset:23552
	v_add_f32_e32 v17, v19, v83
	v_mul_f32_e32 v16, 0x4038aa3b, v16
	s_waitcnt lgkmcnt(1)
	v_mfma_f32_16x16x32_f16 v[22:25], v[30:33], v[70:73], v[22:25]
	ds_read_b128 v[30:33], v38 offset:24576
	v_mul_f32_e32 v17, 0x4038aa3b, v17
	v_exp_f32_e32 v16, v16
	s_waitcnt lgkmcnt(1)
	v_mfma_f32_16x16x32_f16 v[22:25], v[26:29], v[74:77], v[22:25]
	ds_read_b128 v[26:29], v38 offset:25600
	v_exp_f32_e32 v17, v17
	v_fmac_f32_e32 v14, v15, v89
	s_waitcnt lgkmcnt(1)
	v_mfma_f32_16x16x32_f16 v[30:33], v[30:33], v[46:49], 0
	v_add_f32_e32 v15, 1.0, v16
	v_add_f32_e32 v16, 1.0, v17
	v_add_f32_e32 v17, v20, v84
	s_waitcnt lgkmcnt(0)
	v_mfma_f32_16x16x32_f16 v[26:29], v[26:29], v[50:53], v[30:33]
	v_rcp_f32_e32 v15, v15
	s_nop 1
	ds_read_b128 v[30:33], v38 offset:27648
	v_mul_f32_e32 v17, 0x4038aa3b, v17
	v_mfma_f32_16x16x32_f16 v[26:29], v[34:37], v[54:57], v[26:29]
	ds_read_b128 v[34:37], v38 offset:28672
	v_rcp_f32_e32 v16, v16
	v_exp_f32_e32 v17, v17
	s_waitcnt lgkmcnt(1)
	v_mfma_f32_16x16x32_f16 v[26:29], v[30:33], v[58:61], v[26:29]
	ds_read_b128 v[30:33], v38 offset:29696
	v_fma_f32 v15, v15, -2.0, 1.0
	s_waitcnt vmcnt(4)
	v_fmac_f32_e32 v14, v15, v90
	v_fma_f32 v15, v16, -2.0, 1.0
	v_add_f32_e32 v16, 1.0, v17
	v_add_f32_e32 v17, v21, v85
	s_waitcnt lgkmcnt(1)
	v_mfma_f32_16x16x32_f16 v[26:29], v[34:37], v[62:65], v[26:29]
	ds_read_b128 v[34:37], v38 offset:30720
	v_rcp_f32_e32 v16, v16
	v_mul_f32_e32 v17, 0x4038aa3b, v17
	v_exp_f32_e32 v17, v17
	s_waitcnt lgkmcnt(1)
	v_mfma_f32_16x16x32_f16 v[26:29], v[30:33], v[66:69], v[26:29]
	ds_read_b128 v[30:33], v38 offset:31744
	v_fmac_f32_e32 v14, v15, v91
	v_fma_f32 v15, v16, -2.0, 1.0
	s_waitcnt vmcnt(3)
	v_add_f32_e32 v16, v22, v94
	v_fmac_f32_e32 v14, v15, v92
	v_add_f32_e32 v15, 1.0, v17
	v_mul_f32_e32 v16, 0x4038aa3b, v16
	v_add_f32_e32 v17, v23, v95
	v_exp_f32_e32 v16, v16
	v_mul_f32_e32 v17, 0x4038aa3b, v17
	v_exp_f32_e32 v17, v17
	s_waitcnt lgkmcnt(1)
	v_mfma_f32_16x16x32_f16 v[26:29], v[34:37], v[70:73], v[26:29]
	v_rcp_f32_e32 v15, v15
	v_add_f32_e32 v16, 1.0, v16
	v_rcp_f32_e32 v16, v16
	v_add_f32_e32 v17, 1.0, v17
	v_rcp_f32_e32 v17, v17
	s_waitcnt lgkmcnt(0)
	v_mfma_f32_16x16x32_f16 v[26:29], v[30:33], v[74:77], v[26:29]
	v_fma_f32 v15, v15, -2.0, 1.0
	v_fmac_f32_e32 v14, v15, v93
	v_fma_f32 v15, v16, -2.0, 1.0
	v_add_f32_e32 v16, v24, v96
	s_waitcnt vmcnt(1)
	v_fmac_f32_e32 v14, v15, v98
	v_fma_f32 v15, v17, -2.0, 1.0
	v_mul_f32_e32 v16, 0x4038aa3b, v16
	v_add_f32_e32 v17, v25, v97
	v_exp_f32_e32 v16, v16
	v_mul_f32_e32 v17, 0x4038aa3b, v17
	v_add_f32_e32 v6, v26, v6
	v_exp_f32_e32 v17, v17
	v_mul_f32_e32 v6, 0x4038aa3b, v6
	v_exp_f32_e32 v6, v6
	v_fmac_f32_e32 v14, v15, v99
	v_add_f32_e32 v15, 1.0, v16
	v_rcp_f32_e32 v15, v15
	v_add_f32_e32 v16, 1.0, v17
	v_rcp_f32_e32 v16, v16
	v_add_f32_e32 v6, 1.0, v6
	v_rcp_f32_e32 v6, v6
	v_add_f32_e32 v7, v27, v7
	v_mul_f32_e32 v7, 0x4038aa3b, v7
	v_fma_f32 v15, v15, -2.0, 1.0
	v_exp_f32_e32 v7, v7
	v_fmac_f32_e32 v14, v15, v100
	v_fma_f32 v15, v16, -2.0, 1.0
	v_fmac_f32_e32 v14, v15, v101
	v_fma_f32 v6, v6, -2.0, 1.0
	s_waitcnt vmcnt(0)
	v_fmac_f32_e32 v14, v6, v2
	v_add_f32_e32 v6, v28, v8
	v_add_f32_e32 v2, 1.0, v7
	v_mul_f32_e32 v6, 0x4038aa3b, v6
	v_add_f32_e32 v7, v29, v9
	v_exp_f32_e32 v6, v6
	v_mul_f32_e32 v7, 0x4038aa3b, v7
	v_exp_f32_e32 v7, v7
	v_rcp_f32_e32 v2, v2
	v_add_f32_e32 v6, 1.0, v6
	v_rcp_f32_e32 v6, v6
	v_add_f32_e32 v7, 1.0, v7
	v_rcp_f32_e32 v7, v7
	v_fma_f32 v2, v2, -2.0, 1.0
	v_fmac_f32_e32 v14, v2, v3
	v_fma_f32 v2, v6, -2.0, 1.0
	v_fmac_f32_e32 v14, v2, v4
	v_fma_f32 v2, v7, -2.0, 1.0
	v_fmac_f32_e32 v14, v2, v5
	v_mov_b32_e32 v2, v14
	s_nop 1
	v_permlane16_swap_b32_e32 v14, v2
	v_add_f32_e32 v2, v14, v2
	v_mov_b32_e32 v3, v2
	s_nop 1
	v_permlane32_swap_b32_e32 v2, v3
	v_add_f32_e32 v2, v2, v3
	s_and_saveexec_b64 s[4:5], s[8:9]
	v_lshl_or_b32 v3, v11, 6, v0
	v_add_u32_e32 v3, 0x10000, v3
	ds_write_b32 v3, v2
	s_or_b64 exec, exec, s[4:5]
	v_cmp_eq_u32_e64 s[4:5], 0, v12
	s_and_b64 s[2:3], s[4:5], s[2:3]
	s_and_b64 s[2:3], s[2:3], vcc
	s_waitcnt lgkmcnt(0)
	s_barrier
	s_and_saveexec_b64 s[4:5], s[2:3]
	s_cbranch_execz .LBB1_4
	v_lshl_or_b32 v0, v11, 6, v0
	v_add_u32_e32 v0, 0x10000, v0
	ds_read_b32 v0, v0
	s_load_dwordx2 s[0:1], s[0:1], 0x30
	s_movk_i32 s2, 0xc8
	s_waitcnt lgkmcnt(0)
	v_add_f32_e32 v0, v2, v0
	v_add_f32_e32 v0, s6, v0
	v_mul_f32_e32 v0, 0xbfb8aa3b, v0
	v_exp_f32_e32 v0, v0
	s_nop 0
	v_add_f32_e32 v0, 1.0, v0
	v_rcp_f32_e32 v2, v0
	v_mad_u64_u32 v[0:1], s[2:3], v1, s2, v[10:11]
	v_ashrrev_i32_e32 v1, 31, v0
	v_lshl_add_u64 v[0:1], v[0:1], 2, s[0:1]
	global_store_dword v[0:1], v2, off

	.amdhsa_kernel _Z2kBPKfPKDv4_jPKDF16_S0_S0_S0_Pf
		.amdhsa_group_segment_fixed_size 65792
		.amdhsa_private_segment_fixed_size 0
		.amdhsa_kernarg_size 56
		.amdhsa_user_sgpr_count 2
		.amdhsa_user_sgpr_dispatch_ptr 0
		.amdhsa_user_sgpr_queue_ptr 0
		.amdhsa_user_sgpr_kernarg_segment_ptr 1
		.amdhsa_user_sgpr_dispatch_id 0
		.amdhsa_user_sgpr_kernarg_preload_length 0
		.amdhsa_user_sgpr_kernarg_preload_offset 0
		.amdhsa_user_sgpr_private_segment_size 0
		.amdhsa_uses_dynamic_stack 0
		.amdhsa_enable_private_segment 0
		.amdhsa_system_sgpr_workgroup_id_x 1
		.amdhsa_system_sgpr_workgroup_id_y 0
		.amdhsa_system_sgpr_workgroup_id_z 0
		.amdhsa_system_sgpr_workgroup_info 0
		.amdhsa_system_vgpr_workitem_id 0
		.amdhsa_next_free_vgpr 126
		.amdhsa_next_free_sgpr 96
		.amdhsa_accum_offset 128
		.amdhsa_reserve_vcc 1
		.amdhsa_float_round_mode_32 0
		.amdhsa_float_round_mode_16_64 0
		.amdhsa_float_denorm_mode_32 3
		.amdhsa_float_denorm_mode_16_64 3
		.amdhsa_dx10_clamp 1
		.amdhsa_ieee_mode 1
		.amdhsa_fp16_overflow 0
		.amdhsa_tg_split 0
		.amdhsa_exception_fp_ieee_invalid_op 0
		.amdhsa_exception_fp_denorm_src 0
		.amdhsa_exception_fp_ieee_div_zero 0
		.amdhsa_exception_fp_ieee_overflow 0
		.amdhsa_exception_fp_ieee_underflow 0
		.amdhsa_exception_fp_ieee_inexact 0
		.amdhsa_exception_int_div_zero 0
	.end_amdhsa_kernel

amdhsa.kernels:
  - .agpr_count:     0
    .args:
      - .offset:         0
        .size:           120
        .value_kind:     by_value
    .group_segment_fixed_size: 84608
    .kernarg_segment_align: 8
    .kernarg_segment_size: 120
    .language:       OpenCL C
    .language_version:
      - 2
      - 0
    .max_flat_workgroup_size: 512
    .name:           _Z2kA5AArgs
    .private_segment_fixed_size: 0
    .sgpr_count:     50
    .sgpr_spill_count: 0
    .symbol:         _Z2kA5AArgs.kd
    .uniform_work_group_size: 1
    .uses_dynamic_stack: false
    .vgpr_count:     224
    .vgpr_spill_count: 0
    .wavefront_size: 64
  - .agpr_count:     0
    .args:
      - .actual_access:  read_only
        .address_space:  global
        .offset:         0
        .size:           8
        .value_kind:     global_buffer
      - .actual_access:  read_only
        .address_space:  global
        .offset:         8
        .size:           8
        .value_kind:     global_buffer
      - .actual_access:  read_only
        .address_space:  global
        .offset:         16
        .size:           8
        .value_kind:     global_buffer
      - .actual_access:  read_only
        .address_space:  global
        .offset:         24
        .size:           8
        .value_kind:     global_buffer
      - .actual_access:  read_only
        .address_space:  global
        .offset:         32
        .size:           8
        .value_kind:     global_buffer
      - .actual_access:  read_only
        .address_space:  global
        .offset:         40
        .size:           8
        .value_kind:     global_buffer
      - .actual_access:  write_only
        .address_space:  global
        .offset:         48
        .size:           8
        .value_kind:     global_buffer
    .group_segment_fixed_size: 65792
    .kernarg_segment_align: 8
    .kernarg_segment_size: 56
    .language:       OpenCL C
    .language_version:
      - 2
      - 0
    .max_flat_workgroup_size: 512
    .name:           _Z2kBPKfPKDv4_jPKDF16_S0_S0_S0_Pf
    .private_segment_fixed_size: 0
    .sgpr_count:     18
    .sgpr_spill_count: 0
    .symbol:         _Z2kBPKfPKDv4_jPKDF16_S0_S0_S0_Pf.kd
    .uniform_work_group_size: 1
    .uses_dynamic_stack: false
    .vgpr_count:     126
    .vgpr_spill_count: 0
    .wavefront_size: 64
